# MoE K-loop: compiler-inserted vmcnt(0) after the counted vmcnt(7) relaxed to vmcnt(7) (prefetch stays 2 steps deep); drain moved to loop exit
# speedup vs baseline: 1.0655x; 1.0655x over previous
.LBB0_3326:
	s_add_i32 s15, s16, 2
	s_add_i32 s16, s16, 4
	s_min_u32 s16, s16, 63
	s_mul_i32 s17, s14, 0xa000
	s_lshl_b32 s64, s16, 6
	s_add_i32 s20, s17, 0xffff6000
	s_cmp_lg_u32 s14, 0
	s_cselect_b32 s20, s20, 0x14000
	s_add_i32 s20, s18, s20
	s_waitcnt lgkmcnt(0)
	s_barrier
	v_lshl_add_u64 v[156:157], v[202:203], 0, s[64:65]
	s_mov_b32 m0, s20
	s_nop 0
	global_load_lds_dwordx4 v[156:157], off
	v_lshl_add_u64 v[156:157], v[204:205], 0, s[64:65]
	s_add_i32 m0, s20, 0x400
	s_nop 0
	global_load_lds_dwordx4 v[156:157], off
	v_lshl_add_u64 v[156:157], v[206:207], 0, s[64:65]
	s_add_i32 m0, s20, 0x800
	s_nop 0
	global_load_lds_dwordx4 v[156:157], off
	v_lshl_add_u64 v[156:157], v[208:209], 0, s[64:65]
	s_add_i32 m0, s20, 0xc00
	s_nop 0
	global_load_lds_dwordx4 v[156:157], off
	v_lshl_add_u64 v[156:157], v[210:211], 0, s[64:65]
	s_add_i32 m0, s20, 0x1000
	s_lshl_b32 s64, s16, 16
	global_load_lds_dwordx4 v[156:157], off
	v_lshl_add_u64 v[160:161], v[212:213], 0, s[64:65]
	global_load_dwordx4 v[156:159], v[160:161], off nt
	s_nop 0
	global_load_dwordx4 v[160:163], v[160:161], off offset:2048 nt
	v_add_u32_e32 v167, s17, v86
	ds_read2_b32 v[168:169], v201 offset0:0 offset1:0x84
	ds_read2_b32 v[170:171], v232 offset0:0 offset1:0x84
	ds_read2_b32 v[172:173], v201 offset0:16 offset1:0x94
	ds_read2_b32 v[174:175], v232 offset0:16 offset1:0x94
	ds_read2_b32 v[176:177], v201 offset0:32 offset1:0xa4
	ds_read2_b32 v[178:179], v232 offset0:32 offset1:0xa4
	ds_read2_b32 v[180:181], v201 offset0:48 offset1:0xb4
	ds_read2_b32 v[182:183], v232 offset0:48 offset1:0xb4
	ds_read_b128 v[184:187], v167 offset:0
	ds_read_b128 v[188:191], v167 offset:0x400
	s_nop 0
	s_waitcnt lgkmcnt(1)
	s_setprio 1
	v_mfma_f32_16x16x32_bf16 v[140:143], v[168:171], v[184:187], v[140:143]
	v_mfma_f32_16x16x32_bf16 v[132:135], v[172:175], v[184:187], v[132:135]
	v_mfma_f32_16x16x32_bf16 v[144:147], v[176:179], v[184:187], v[144:147]
	v_mfma_f32_16x16x32_bf16 v[136:139], v[180:183], v[184:187], v[136:139]
	ds_read_b128 v[184:187], v167 offset:0x800
	s_waitcnt lgkmcnt(1)
	s_nop 0
	v_mfma_f32_16x16x32_bf16 v[124:127], v[168:171], v[188:191], v[124:127]
	v_mfma_f32_16x16x32_bf16 v[112:115], v[172:175], v[188:191], v[112:115]
	v_mfma_f32_16x16x32_bf16 v[128:131], v[176:179], v[188:191], v[128:131]
	v_mfma_f32_16x16x32_bf16 v[116:119], v[180:183], v[188:191], v[116:119]
	ds_read_b128 v[188:191], v167 offset:0xc00
	s_waitcnt lgkmcnt(1)
	s_nop 0
	v_mfma_f32_16x16x32_bf16 v[82:85], v[168:171], v[184:187], v[82:85]
	v_mfma_f32_16x16x32_bf16 v[54:57], v[172:175], v[184:187], v[54:57]
	v_mfma_f32_16x16x32_bf16 v[88:91], v[176:179], v[184:187], v[88:91]
	v_mfma_f32_16x16x32_bf16 v[58:61], v[180:183], v[184:187], v[58:61]
	ds_read_b128 v[184:187], v167 offset:0x1000
	s_waitcnt lgkmcnt(1)
	s_nop 0
	v_mfma_f32_16x16x32_bf16 v[26:29], v[168:171], v[188:191], v[26:29]
	v_mfma_f32_16x16x32_bf16 v[6:9], v[172:175], v[188:191], v[6:9]
	v_mfma_f32_16x16x32_bf16 v[42:45], v[176:179], v[188:191], v[42:45]
	v_mfma_f32_16x16x32_bf16 v[14:17], v[180:183], v[188:191], v[14:17]
	ds_read_b128 v[188:191], v167 offset:0x1400
	s_waitcnt lgkmcnt(1)
	s_nop 0
	v_mfma_f32_16x16x32_bf16 v[92:95], v[168:171], v[184:187], v[92:95]
	v_mfma_f32_16x16x32_bf16 v[62:65], v[172:175], v[184:187], v[62:65]
	v_mfma_f32_16x16x32_bf16 v[96:99], v[176:179], v[184:187], v[96:99]
	v_mfma_f32_16x16x32_bf16 v[66:69], v[180:183], v[184:187], v[66:69]
	ds_read_b128 v[184:187], v167 offset:0x1800
	s_waitcnt lgkmcnt(1)
	s_nop 0
	v_mfma_f32_16x16x32_bf16 v[38:41], v[168:171], v[188:191], v[38:41]
	v_mfma_f32_16x16x32_bf16 v[18:21], v[172:175], v[188:191], v[18:21]
	v_mfma_f32_16x16x32_bf16 v[46:49], v[176:179], v[188:191], v[46:49]
	v_mfma_f32_16x16x32_bf16 v[22:25], v[180:183], v[188:191], v[22:25]
	ds_read_b128 v[188:191], v167 offset:0x1c00
	s_waitcnt lgkmcnt(1)
	s_nop 0
	v_mfma_f32_16x16x32_bf16 v[108:111], v[168:171], v[184:187], v[108:111]
	s_waitcnt lgkmcnt(0)
	v_mfma_f32_16x16x32_bf16 v[100:103], v[172:175], v[184:187], v[100:103]
	v_mfma_f32_16x16x32_bf16 v[120:123], v[176:179], v[184:187], v[120:123]
	v_mfma_f32_16x16x32_bf16 v[104:107], v[180:183], v[184:187], v[104:107]
	v_mfma_f32_16x16x32_bf16 v[70:73], v[168:171], v[188:191], v[70:73]
	v_mfma_f32_16x16x32_bf16 v[50:53], v[172:175], v[188:191], v[50:53]
	v_mfma_f32_16x16x32_bf16 v[10:13], v[176:179], v[188:191], v[10:13]
	v_mfma_f32_16x16x32_bf16 v[2:5], v[180:183], v[188:191], v[2:5]
	s_setprio 0
	s_add_i32 s16, s14, 1
	s_cmp_lg_u32 s14, 2
	s_cselect_b32 s14, s16, 0
	s_min_u32 s16, s15, 60
	s_add_i32 s16, s16, 3
	s_mul_i32 s17, s14, 0xa000
	s_lshl_b32 s64, s16, 6
	s_add_i32 s20, s17, 0xffff6000
	s_cmp_lg_u32 s14, 0
	s_waitcnt vmcnt(7)
	v_cvt_pk_bf16_f32 v148, v152, v148
	v_add_u32_e32 v152, 0x20100, v165
	s_cselect_b32 s20, s20, 0x14000
	v_cvt_pk_bf16_f32 v149, v153, v149
	v_cvt_pk_bf16_f32 v150, v154, v150
	v_cvt_pk_bf16_f32 v151, v155, v151
	ds_write_b128 v152, v[148:151]
	v_lshl_add_u64 v[168:169], v[202:203], 0, s[64:65]
	v_lshl_add_u64 v[170:171], v[204:205], 0, s[64:65]
	v_lshl_add_u64 v[172:173], v[206:207], 0, s[64:65]
	v_lshl_add_u64 v[174:175], v[208:209], 0, s[64:65]
	v_lshl_add_u64 v[176:177], v[210:211], 0, s[64:65]
	s_lshl_b32 s64, s16, 16
	s_add_i32 s16, s18, s20
	s_waitcnt lgkmcnt(0)
	s_barrier
	v_lshl_add_u64 v[148:149], v[212:213], 0, s[64:65]
	s_mov_b32 m0, s16
	global_load_dwordx4 v[152:155], v[148:149], off nt
	s_nop 0
	global_load_dwordx4 v[148:151], v[148:149], off offset:2048 nt
	s_nop 0
	global_load_lds_dwordx4 v[168:169], off
	s_add_i32 m0, s16, 0x400
	s_nop 0
	global_load_lds_dwordx4 v[170:171], off
	s_add_i32 m0, s16, 0x800
	s_nop 0
	global_load_lds_dwordx4 v[172:173], off
	s_add_i32 m0, s16, 0xc00
	s_nop 0
	global_load_lds_dwordx4 v[174:175], off
	s_add_i32 m0, s16, 0x1000
	s_nop 0
	global_load_lds_dwordx4 v[176:177], off
	v_add_u32_e32 v167, s17, v86
	ds_read2_b32 v[168:169], v233 offset0:0 offset1:0x84
	ds_read2_b32 v[170:171], v234 offset0:0 offset1:0x84
	ds_read2_b32 v[172:173], v233 offset0:16 offset1:0x94
	ds_read2_b32 v[174:175], v234 offset0:16 offset1:0x94
	ds_read2_b32 v[176:177], v233 offset0:32 offset1:0xa4
	ds_read2_b32 v[178:179], v234 offset0:32 offset1:0xa4
	ds_read2_b32 v[180:181], v233 offset0:48 offset1:0xb4
	ds_read2_b32 v[182:183], v234 offset0:48 offset1:0xb4
	ds_read_b128 v[184:187], v167 offset:0
	ds_read_b128 v[188:191], v167 offset:0x400
	s_nop 0
	s_waitcnt lgkmcnt(1)
	s_setprio 1
	v_mfma_f32_16x16x32_bf16 v[140:143], v[168:171], v[184:187], v[140:143]
	v_mfma_f32_16x16x32_bf16 v[132:135], v[172:175], v[184:187], v[132:135]
	v_mfma_f32_16x16x32_bf16 v[144:147], v[176:179], v[184:187], v[144:147]
	v_mfma_f32_16x16x32_bf16 v[136:139], v[180:183], v[184:187], v[136:139]
	ds_read_b128 v[184:187], v167 offset:0x800
	s_waitcnt lgkmcnt(1)
	s_nop 0
	v_mfma_f32_16x16x32_bf16 v[124:127], v[168:171], v[188:191], v[124:127]
	v_mfma_f32_16x16x32_bf16 v[112:115], v[172:175], v[188:191], v[112:115]
	v_mfma_f32_16x16x32_bf16 v[128:131], v[176:179], v[188:191], v[128:131]
	v_mfma_f32_16x16x32_bf16 v[116:119], v[180:183], v[188:191], v[116:119]
	ds_read_b128 v[188:191], v167 offset:0xc00
	s_waitcnt lgkmcnt(1)
	s_nop 0
	v_mfma_f32_16x16x32_bf16 v[82:85], v[168:171], v[184:187], v[82:85]
	v_mfma_f32_16x16x32_bf16 v[54:57], v[172:175], v[184:187], v[54:57]
	v_mfma_f32_16x16x32_bf16 v[88:91], v[176:179], v[184:187], v[88:91]
	v_mfma_f32_16x16x32_bf16 v[58:61], v[180:183], v[184:187], v[58:61]
	ds_read_b128 v[184:187], v167 offset:0x1000
	s_waitcnt lgkmcnt(1)
	s_nop 0
	v_mfma_f32_16x16x32_bf16 v[26:29], v[168:171], v[188:191], v[26:29]
	v_mfma_f32_16x16x32_bf16 v[6:9], v[172:175], v[188:191], v[6:9]
	v_mfma_f32_16x16x32_bf16 v[42:45], v[176:179], v[188:191], v[42:45]
	v_mfma_f32_16x16x32_bf16 v[14:17], v[180:183], v[188:191], v[14:17]
	ds_read_b128 v[188:191], v167 offset:0x1400
	s_waitcnt lgkmcnt(1)
	s_nop 0
	v_mfma_f32_16x16x32_bf16 v[92:95], v[168:171], v[184:187], v[92:95]
	v_mfma_f32_16x16x32_bf16 v[62:65], v[172:175], v[184:187], v[62:65]
	v_mfma_f32_16x16x32_bf16 v[96:99], v[176:179], v[184:187], v[96:99]
	v_mfma_f32_16x16x32_bf16 v[66:69], v[180:183], v[184:187], v[66:69]
	ds_read_b128 v[184:187], v167 offset:0x1800
	s_waitcnt lgkmcnt(1)
	s_nop 0
	v_mfma_f32_16x16x32_bf16 v[38:41], v[168:171], v[188:191], v[38:41]
	v_mfma_f32_16x16x32_bf16 v[18:21], v[172:175], v[188:191], v[18:21]
	v_mfma_f32_16x16x32_bf16 v[46:49], v[176:179], v[188:191], v[46:49]
	v_mfma_f32_16x16x32_bf16 v[22:25], v[180:183], v[188:191], v[22:25]
	ds_read_b128 v[188:191], v167 offset:0x1c00
	s_waitcnt lgkmcnt(1)
	s_nop 0
	v_mfma_f32_16x16x32_bf16 v[108:111], v[168:171], v[184:187], v[108:111]
	s_waitcnt lgkmcnt(0)
	v_mfma_f32_16x16x32_bf16 v[100:103], v[172:175], v[184:187], v[100:103]
	v_mfma_f32_16x16x32_bf16 v[120:123], v[176:179], v[184:187], v[120:123]
	v_mfma_f32_16x16x32_bf16 v[104:107], v[180:183], v[184:187], v[104:107]
	v_mfma_f32_16x16x32_bf16 v[70:73], v[168:171], v[188:191], v[70:73]
	v_mfma_f32_16x16x32_bf16 v[50:53], v[172:175], v[188:191], v[50:53]
	v_mfma_f32_16x16x32_bf16 v[10:13], v[176:179], v[188:191], v[10:13]
	v_mfma_f32_16x16x32_bf16 v[2:5], v[180:183], v[188:191], v[2:5]
	s_setprio 0
	s_waitcnt vmcnt(7)
	s_add_i32 s16, s14, 1
	s_cmp_lg_u32 s14, 2
	s_cselect_b32 s14, s16, 0
	s_cmp_gt_u32 s15, 61
	s_mov_b32 s16, s15
	s_waitcnt vmcnt(7)
	v_cvt_pk_bf16_f32 v156, v156, v160
	v_cvt_pk_bf16_f32 v157, v157, v161
	v_cvt_pk_bf16_f32 v158, v158, v162
	v_cvt_pk_bf16_f32 v159, v159, v163
	ds_write_b128 v166, v[156:159]
	s_cbranch_scc0 .LBB0_3326
	s_waitcnt vmcnt(0)
	s_mov_b64 s[14:15], 0
	s_branch .LBB0_3333

.LBB0_3331:
	s_add_i32 s17, s20, 2
	s_add_i32 s20, s20, 4
	s_min_u32 s20, s20, 63
	s_mul_i32 s21, s16, 0xa000
	s_lshl_b32 s64, s20, 6
	s_add_i32 s22, s21, 0xffff6000
	s_cmp_lg_u32 s16, 0
	s_cselect_b32 s22, s22, 0x14000
	s_add_i32 s22, s18, s22
	s_waitcnt lgkmcnt(0)
	s_barrier
	v_lshl_add_u64 v[52:53], v[202:203], 0, s[64:65]
	s_mov_b32 m0, s22
	s_nop 0
	global_load_lds_dwordx4 v[52:53], off
	v_lshl_add_u64 v[52:53], v[204:205], 0, s[64:65]
	s_add_i32 m0, s22, 0x400
	s_nop 0
	global_load_lds_dwordx4 v[52:53], off
	v_lshl_add_u64 v[52:53], v[206:207], 0, s[64:65]
	s_add_i32 m0, s22, 0x800
	s_nop 0
	global_load_lds_dwordx4 v[52:53], off
	v_lshl_add_u64 v[52:53], v[208:209], 0, s[64:65]
	s_add_i32 m0, s22, 0xc00
	s_nop 0
	global_load_lds_dwordx4 v[52:53], off
	v_lshl_add_u64 v[52:53], v[210:211], 0, s[64:65]
	s_add_i32 m0, s22, 0x1000
	s_lshl_b32 s64, s20, 16
	global_load_lds_dwordx4 v[52:53], off
	v_lshl_add_u64 v[52:53], v[212:213], 0, s[64:65]
	global_load_dwordx4 v[70:73], v[52:53], off nt
	global_load_dwordx4 v[100:103], v[52:53], off offset:2048 nt
	v_add_u32_e32 v160, s21, v86
	ds_read2_b32 v[104:105], v201 offset0:0 offset1:0x84
	ds_read2_b32 v[106:107], v232 offset0:0 offset1:0x84
	ds_read2_b32 v[108:109], v201 offset0:16 offset1:0x94
	ds_read2_b32 v[110:111], v232 offset0:16 offset1:0x94
	ds_read2_b32 v[120:121], v201 offset0:32 offset1:0xa4
	ds_read2_b32 v[122:123], v232 offset0:32 offset1:0xa4
	ds_read2_b32 v[148:149], v201 offset0:48 offset1:0xb4
	ds_read2_b32 v[150:151], v232 offset0:48 offset1:0xb4
	ds_read_b128 v[152:155], v160 offset:0
	ds_read_b128 v[156:159], v160 offset:0x400
	s_nop 0
	s_waitcnt lgkmcnt(1)
	s_setprio 1
	v_mfma_f32_16x16x32_bf16 v[140:143], v[104:107], v[152:155], v[140:143]
	v_mfma_f32_16x16x32_bf16 v[132:135], v[108:111], v[152:155], v[132:135]
	v_mfma_f32_16x16x32_bf16 v[144:147], v[120:123], v[152:155], v[144:147]
	v_mfma_f32_16x16x32_bf16 v[136:139], v[148:151], v[152:155], v[136:139]
	ds_read_b128 v[152:155], v160 offset:0x800
	s_waitcnt lgkmcnt(1)
	s_nop 0
	v_mfma_f32_16x16x32_bf16 v[124:127], v[104:107], v[156:159], v[124:127]
	v_mfma_f32_16x16x32_bf16 v[112:115], v[108:111], v[156:159], v[112:115]
	v_mfma_f32_16x16x32_bf16 v[128:131], v[120:123], v[156:159], v[128:131]
	v_mfma_f32_16x16x32_bf16 v[116:119], v[148:151], v[156:159], v[116:119]
	ds_read_b128 v[156:159], v160 offset:0xc00
	s_waitcnt lgkmcnt(1)
	s_nop 0
	v_mfma_f32_16x16x32_bf16 v[82:85], v[104:107], v[152:155], v[82:85]
	v_mfma_f32_16x16x32_bf16 v[52:55], v[108:111], v[152:155], v[54:57]
	v_mfma_f32_16x16x32_bf16 v[88:91], v[120:123], v[152:155], v[88:91]
	v_mfma_f32_16x16x32_bf16 v[58:61], v[148:151], v[152:155], v[58:61]
	ds_read_b128 v[152:155], v160 offset:0x1000
	s_waitcnt lgkmcnt(1)
	s_nop 0
	v_mfma_f32_16x16x32_bf16 v[26:29], v[104:107], v[156:159], v[26:29]
	v_mfma_f32_16x16x32_bf16 v[6:9], v[108:111], v[156:159], v[6:9]
	v_mfma_f32_16x16x32_bf16 v[42:45], v[120:123], v[156:159], v[42:45]
	v_mfma_f32_16x16x32_bf16 v[14:17], v[148:151], v[156:159], v[14:17]
	ds_read_b128 v[156:159], v160 offset:0x1400
	s_waitcnt lgkmcnt(1)
	s_nop 0
	v_mfma_f32_16x16x32_bf16 v[92:95], v[104:107], v[152:155], v[92:95]
	s_waitcnt lgkmcnt(0)
	v_mfma_f32_16x16x32_bf16 v[62:65], v[108:111], v[152:155], v[62:65]
	v_mfma_f32_16x16x32_bf16 v[96:99], v[120:123], v[152:155], v[96:99]
	v_mfma_f32_16x16x32_bf16 v[66:69], v[148:151], v[152:155], v[66:69]
	v_mfma_f32_16x16x32_bf16 v[38:41], v[104:107], v[156:159], v[38:41]
	v_mfma_f32_16x16x32_bf16 v[18:21], v[108:111], v[156:159], v[18:21]
	v_mfma_f32_16x16x32_bf16 v[46:49], v[120:123], v[156:159], v[46:49]
	v_mfma_f32_16x16x32_bf16 v[22:25], v[148:151], v[156:159], v[22:25]
	s_setprio 0
	s_add_i32 s20, s16, 1
	s_cmp_lg_u32 s16, 2
	s_cselect_b32 s16, s20, 0
	s_min_u32 s20, s17, 60
	s_add_i32 s20, s20, 3
	s_mul_i32 s21, s16, 0xa000
	s_lshl_b32 s64, s20, 6
	s_add_i32 s22, s21, 0xffff6000
	s_cmp_lg_u32 s16, 0
	s_waitcnt vmcnt(7)
	v_cvt_pk_bf16_f32 v2, v10, v2
	v_add_u32_e32 v10, 0x20100, v50
	s_cselect_b32 s22, s22, 0x14000
	v_cvt_pk_bf16_f32 v3, v11, v3
	v_cvt_pk_bf16_f32 v4, v12, v4
	v_cvt_pk_bf16_f32 v5, v13, v5
	ds_write_b128 v10, v[2:5]
	v_lshl_add_u64 v[56:57], v[202:203], 0, s[64:65]
	v_lshl_add_u64 v[104:105], v[204:205], 0, s[64:65]
	v_lshl_add_u64 v[106:107], v[206:207], 0, s[64:65]
	v_lshl_add_u64 v[108:109], v[208:209], 0, s[64:65]
	v_lshl_add_u64 v[110:111], v[210:211], 0, s[64:65]
	s_lshl_b32 s64, s20, 16
	s_add_i32 s20, s18, s22
	s_waitcnt lgkmcnt(0)
	s_barrier
	v_lshl_add_u64 v[2:3], v[212:213], 0, s[64:65]
	s_mov_b32 m0, s20
	global_load_dwordx4 v[10:13], v[2:3], off nt
	s_nop 0
	global_load_dwordx4 v[2:5], v[2:3], off offset:2048 nt
	s_nop 0
	global_load_lds_dwordx4 v[56:57], off
	s_add_i32 m0, s20, 0x400
	s_nop 0
	global_load_lds_dwordx4 v[104:105], off
	s_add_i32 m0, s20, 0x800
	s_nop 0
	global_load_lds_dwordx4 v[106:107], off
	s_add_i32 m0, s20, 0xc00
	s_nop 0
	global_load_lds_dwordx4 v[108:109], off
	s_add_i32 m0, s20, 0x1000
	s_nop 0
	global_load_lds_dwordx4 v[110:111], off
	v_add_u32_e32 v160, s21, v86
	ds_read2_b32 v[104:105], v233 offset0:0 offset1:0x84
	ds_read2_b32 v[106:107], v234 offset0:0 offset1:0x84
	ds_read2_b32 v[108:109], v233 offset0:16 offset1:0x94
	ds_read2_b32 v[110:111], v234 offset0:16 offset1:0x94
	ds_read2_b32 v[120:121], v233 offset0:32 offset1:0xa4
	ds_read2_b32 v[122:123], v234 offset0:32 offset1:0xa4
	ds_read2_b32 v[148:149], v233 offset0:48 offset1:0xb4
	ds_read2_b32 v[150:151], v234 offset0:48 offset1:0xb4
	ds_read_b128 v[152:155], v160 offset:0
	ds_read_b128 v[156:159], v160 offset:0x400
	s_nop 0
	s_waitcnt lgkmcnt(1)
	s_setprio 1
	v_mfma_f32_16x16x32_bf16 v[140:143], v[104:107], v[152:155], v[140:143]
	v_mfma_f32_16x16x32_bf16 v[132:135], v[108:111], v[152:155], v[132:135]
	v_mfma_f32_16x16x32_bf16 v[144:147], v[120:123], v[152:155], v[144:147]
	v_mfma_f32_16x16x32_bf16 v[136:139], v[148:151], v[152:155], v[136:139]
	ds_read_b128 v[152:155], v160 offset:0x800
	s_waitcnt lgkmcnt(1)
	s_nop 0
	v_mfma_f32_16x16x32_bf16 v[124:127], v[104:107], v[156:159], v[124:127]
	v_mfma_f32_16x16x32_bf16 v[112:115], v[108:111], v[156:159], v[112:115]
	v_mfma_f32_16x16x32_bf16 v[128:131], v[120:123], v[156:159], v[128:131]
	v_mfma_f32_16x16x32_bf16 v[116:119], v[148:151], v[156:159], v[116:119]
	ds_read_b128 v[156:159], v160 offset:0xc00
	s_waitcnt lgkmcnt(1)
	s_nop 0
	v_mfma_f32_16x16x32_bf16 v[82:85], v[104:107], v[152:155], v[82:85]
	v_mfma_f32_16x16x32_bf16 v[54:57], v[108:111], v[152:155], v[52:55]
	v_mfma_f32_16x16x32_bf16 v[88:91], v[120:123], v[152:155], v[88:91]
	v_mfma_f32_16x16x32_bf16 v[58:61], v[148:151], v[152:155], v[58:61]
	ds_read_b128 v[152:155], v160 offset:0x1000
	s_waitcnt lgkmcnt(1)
	s_nop 0
	v_mfma_f32_16x16x32_bf16 v[26:29], v[104:107], v[156:159], v[26:29]
	v_mfma_f32_16x16x32_bf16 v[6:9], v[108:111], v[156:159], v[6:9]
	v_mfma_f32_16x16x32_bf16 v[42:45], v[120:123], v[156:159], v[42:45]
	v_mfma_f32_16x16x32_bf16 v[14:17], v[148:151], v[156:159], v[14:17]
	ds_read_b128 v[156:159], v160 offset:0x1400
	s_waitcnt lgkmcnt(1)
	s_nop 0
	v_mfma_f32_16x16x32_bf16 v[92:95], v[104:107], v[152:155], v[92:95]
	s_waitcnt lgkmcnt(0)
	v_mfma_f32_16x16x32_bf16 v[62:65], v[108:111], v[152:155], v[62:65]
	v_mfma_f32_16x16x32_bf16 v[96:99], v[120:123], v[152:155], v[96:99]
	v_mfma_f32_16x16x32_bf16 v[66:69], v[148:151], v[152:155], v[66:69]
	v_mfma_f32_16x16x32_bf16 v[38:41], v[104:107], v[156:159], v[38:41]
	v_mfma_f32_16x16x32_bf16 v[18:21], v[108:111], v[156:159], v[18:21]
	v_mfma_f32_16x16x32_bf16 v[46:49], v[120:123], v[156:159], v[46:49]
	v_mfma_f32_16x16x32_bf16 v[22:25], v[148:151], v[156:159], v[22:25]
	s_setprio 0
	s_waitcnt vmcnt(7)
	s_add_i32 s20, s16, 1
	s_cmp_lg_u32 s16, 2
	s_cselect_b32 s16, s20, 0
	s_cmp_gt_u32 s17, 61
	s_mov_b32 s20, s17
	s_waitcnt vmcnt(7)
	v_cvt_pk_bf16_f32 v70, v70, v100
	v_cvt_pk_bf16_f32 v71, v71, v101
	v_cvt_pk_bf16_f32 v72, v72, v102
	v_cvt_pk_bf16_f32 v73, v73, v103
	ds_write_b128 v51, v[70:73]
	s_cbranch_scc0 .LBB0_3331
	s_waitcnt vmcnt(0)
	v_mov_b32_e32 v5, 0
	v_mov_b32_e32 v4, v5
	v_mov_b32_e32 v3, v5
	v_mov_b32_e32 v2, v5
	v_mov_b32_e32 v13, v5
	v_mov_b32_e32 v12, v5
	v_mov_b32_e32 v11, v5
	v_mov_b32_e32 v10, v5
	v_mov_b32_e32 v111, v5
	v_mov_b32_e32 v110, v5
	v_mov_b32_e32 v109, v5
	v_mov_b32_e32 v108, v5
	v_mov_b32_e32 v103, v5
	v_mov_b32_e32 v102, v5
	v_mov_b32_e32 v101, v5
	v_mov_b32_e32 v100, v5
	v_mov_b32_e32 v123, v5
	v_mov_b32_e32 v122, v5
	v_mov_b32_e32 v121, v5
	v_mov_b32_e32 v120, v5
	v_mov_b32_e32 v107, v5
	v_mov_b32_e32 v106, v5
	v_mov_b32_e32 v105, v5
	v_mov_b32_e32 v104, v5
	v_mov_b32_e32 v73, v5
	v_mov_b32_e32 v72, v5
	v_mov_b32_e32 v71, v5
	v_mov_b32_e32 v70, v5
	v_mov_b32_e32 v53, v5
	v_mov_b32_e32 v52, v5
	v_mov_b32_e32 v51, v5
	v_mov_b32_e32 v50, v5

.LBB0_3337:
	s_add_i32 s13, s16, 2
	s_add_i32 s16, s16, 4
	s_min_u32 s16, s16, 63
	s_mul_i32 s17, s12, 0xa000
	s_lshl_b32 s64, s16, 6
	s_add_i32 s20, s17, 0xffff6000
	s_cmp_lg_u32 s12, 0
	s_cselect_b32 s20, s20, 0x14000
	s_add_i32 s20, s18, s20
	s_waitcnt lgkmcnt(0)
	s_barrier
	v_lshl_add_u64 v[20:21], v[202:203], 0, s[64:65]
	s_mov_b32 m0, s20
	s_nop 0
	global_load_lds_dwordx4 v[20:21], off
	v_lshl_add_u64 v[20:21], v[204:205], 0, s[64:65]
	s_add_i32 m0, s20, 0x400
	s_nop 0
	global_load_lds_dwordx4 v[20:21], off
	v_lshl_add_u64 v[20:21], v[206:207], 0, s[64:65]
	s_add_i32 m0, s20, 0x800
	s_nop 0
	global_load_lds_dwordx4 v[20:21], off
	v_lshl_add_u64 v[20:21], v[208:209], 0, s[64:65]
	s_add_i32 m0, s20, 0xc00
	s_nop 0
	global_load_lds_dwordx4 v[20:21], off
	v_lshl_add_u64 v[20:21], v[210:211], 0, s[64:65]
	s_add_i32 m0, s20, 0x1000
	s_lshl_b32 s64, s16, 16
	global_load_lds_dwordx4 v[20:21], off
	v_lshl_add_u64 v[24:25], v[212:213], 0, s[64:65]
	global_load_dwordx4 v[20:23], v[24:25], off nt
	global_load_dwordx4 v[38:41], v[24:25], off offset:2048 nt
	v_add_u32_e32 v24, s17, v86
	ds_read2_b32 v[46:47], v201 offset0:0 offset1:0x84
	ds_read2_b32 v[48:49], v232 offset0:0 offset1:0x84
	ds_read2_b32 v[50:51], v201 offset0:16 offset1:0x94
	ds_read2_b32 v[52:53], v232 offset0:16 offset1:0x94
	ds_read2_b32 v[62:63], v201 offset0:32 offset1:0xa4
	ds_read2_b32 v[64:65], v232 offset0:32 offset1:0xa4
	ds_read2_b32 v[66:67], v201 offset0:48 offset1:0xb4
	ds_read2_b32 v[68:69], v232 offset0:48 offset1:0xb4
	ds_read_b128 v[70:73], v24 offset:0
	ds_read_b128 v[92:95], v24 offset:0x400
	s_nop 0
	s_waitcnt lgkmcnt(1)
	s_setprio 1
	ds_read_b128 v[108:111], v24 offset:0x800
	s_waitcnt lgkmcnt(1)
	v_mfma_f32_16x16x32_bf16 v[96:99], v[46:49], v[70:73], v[140:143]
	v_mfma_f32_16x16x32_bf16 v[120:123], v[46:49], v[92:95], v[124:127]
	v_mfma_f32_16x16x32_bf16 v[112:115], v[50:53], v[92:95], v[112:115]
	v_mfma_f32_16x16x32_bf16 v[128:131], v[62:65], v[92:95], v[128:131]
	v_mfma_f32_16x16x32_bf16 v[92:95], v[66:69], v[92:95], v[116:119]
	ds_read_b128 v[116:119], v24 offset:0xc00
	s_waitcnt lgkmcnt(1)
	s_nop 0
	v_mfma_f32_16x16x32_bf16 v[82:85], v[46:49], v[108:111], v[82:85]
	s_waitcnt lgkmcnt(0)
	v_mfma_f32_16x16x32_bf16 v[54:57], v[50:53], v[108:111], v[54:57]
	v_mfma_f32_16x16x32_bf16 v[88:91], v[62:65], v[108:111], v[88:91]
	v_mfma_f32_16x16x32_bf16 v[58:61], v[66:69], v[108:111], v[58:61]
	v_mfma_f32_16x16x32_bf16 v[24:27], v[46:49], v[116:119], v[26:29]
	v_mfma_f32_16x16x32_bf16 v[6:9], v[50:53], v[116:119], v[6:9]
	v_mfma_f32_16x16x32_bf16 v[42:45], v[62:65], v[116:119], v[42:45]
	v_mfma_f32_16x16x32_bf16 v[14:17], v[66:69], v[116:119], v[14:17]
	v_mfma_f32_16x16x32_bf16 v[100:103], v[50:53], v[70:73], v[132:135]
	v_mfma_f32_16x16x32_bf16 v[104:107], v[62:65], v[70:73], v[144:147]
	v_mfma_f32_16x16x32_bf16 v[70:73], v[66:69], v[70:73], v[136:139]
	s_setprio 0
	s_add_i32 s16, s12, 1
	s_cmp_lg_u32 s12, 2
	s_cselect_b32 s12, s16, 0
	s_min_u32 s16, s13, 60
	s_add_i32 s16, s16, 3
	s_mul_i32 s17, s12, 0xa000
	s_lshl_b32 s64, s16, 6
	s_add_i32 s20, s17, 0xffff6000
	s_cmp_lg_u32 s12, 0
	s_waitcnt vmcnt(7)
	v_cvt_pk_bf16_f32 v2, v10, v2
	v_add_u32_e32 v10, 0x20100, v18
	s_cselect_b32 s20, s20, 0x14000
	v_cvt_pk_bf16_f32 v3, v11, v3
	v_cvt_pk_bf16_f32 v4, v12, v4
	v_cvt_pk_bf16_f32 v5, v13, v5
	ds_write_b128 v10, v[2:5]
	v_lshl_add_u64 v[28:29], v[202:203], 0, s[64:65]
	v_lshl_add_u64 v[46:47], v[204:205], 0, s[64:65]
	v_lshl_add_u64 v[48:49], v[206:207], 0, s[64:65]
	v_lshl_add_u64 v[50:51], v[208:209], 0, s[64:65]
	v_lshl_add_u64 v[52:53], v[210:211], 0, s[64:65]
	s_lshl_b32 s64, s16, 16
	s_add_i32 s16, s18, s20
	s_waitcnt lgkmcnt(0)
	s_barrier
	v_lshl_add_u64 v[2:3], v[212:213], 0, s[64:65]
	s_mov_b32 m0, s16
	global_load_dwordx4 v[10:13], v[2:3], off nt
	s_nop 0
	global_load_dwordx4 v[2:5], v[2:3], off offset:2048 nt
	s_nop 0
	global_load_lds_dwordx4 v[28:29], off
	s_add_i32 m0, s16, 0x400
	s_nop 0
	global_load_lds_dwordx4 v[46:47], off
	s_add_i32 m0, s16, 0x800
	s_nop 0
	global_load_lds_dwordx4 v[48:49], off
	s_add_i32 m0, s16, 0xc00
	s_nop 0
	global_load_lds_dwordx4 v[50:51], off
	s_add_i32 m0, s16, 0x1000
	s_nop 0
	global_load_lds_dwordx4 v[52:53], off
	v_add_u32_e32 v28, s17, v86
	ds_read2_b32 v[46:47], v233 offset0:0 offset1:0x84
	ds_read2_b32 v[48:49], v234 offset0:0 offset1:0x84
	ds_read2_b32 v[50:51], v233 offset0:16 offset1:0x94
	ds_read2_b32 v[52:53], v234 offset0:16 offset1:0x94
	ds_read2_b32 v[62:63], v233 offset0:32 offset1:0xa4
	ds_read2_b32 v[64:65], v234 offset0:32 offset1:0xa4
	ds_read2_b32 v[66:67], v233 offset0:48 offset1:0xb4
	ds_read2_b32 v[68:69], v234 offset0:48 offset1:0xb4
	ds_read_b128 v[108:111], v28 offset:0
	ds_read_b128 v[116:119], v28 offset:0x400
	s_nop 0
	s_waitcnt lgkmcnt(1)
	s_setprio 1
	v_mfma_f32_16x16x32_bf16 v[136:139], v[66:69], v[108:111], v[70:73]
	ds_read_b128 v[70:73], v28 offset:0x800
	s_waitcnt lgkmcnt(1)
	s_nop 0
	v_mfma_f32_16x16x32_bf16 v[124:127], v[46:49], v[116:119], v[120:123]
	v_mfma_f32_16x16x32_bf16 v[112:115], v[50:53], v[116:119], v[112:115]
	v_mfma_f32_16x16x32_bf16 v[128:131], v[62:65], v[116:119], v[128:131]
	v_mfma_f32_16x16x32_bf16 v[116:119], v[66:69], v[116:119], v[92:95]
	ds_read_b128 v[92:95], v28 offset:0xc00
	s_waitcnt lgkmcnt(1)
	v_mfma_f32_16x16x32_bf16 v[140:143], v[46:49], v[108:111], v[96:99]
	s_waitcnt lgkmcnt(0)
	v_mfma_f32_16x16x32_bf16 v[132:135], v[50:53], v[108:111], v[100:103]
	v_mfma_f32_16x16x32_bf16 v[144:147], v[62:65], v[108:111], v[104:107]
	v_mfma_f32_16x16x32_bf16 v[82:85], v[46:49], v[70:73], v[82:85]
	v_mfma_f32_16x16x32_bf16 v[54:57], v[50:53], v[70:73], v[54:57]
	v_mfma_f32_16x16x32_bf16 v[88:91], v[62:65], v[70:73], v[88:91]
	v_mfma_f32_16x16x32_bf16 v[58:61], v[66:69], v[70:73], v[58:61]
	v_mfma_f32_16x16x32_bf16 v[26:29], v[46:49], v[92:95], v[24:27]
	v_mfma_f32_16x16x32_bf16 v[6:9], v[50:53], v[92:95], v[6:9]
	v_mfma_f32_16x16x32_bf16 v[42:45], v[62:65], v[92:95], v[42:45]
	v_mfma_f32_16x16x32_bf16 v[14:17], v[66:69], v[92:95], v[14:17]
	s_setprio 0
	s_waitcnt vmcnt(7)
	s_add_i32 s16, s12, 1
	s_cmp_lg_u32 s12, 2
	s_cselect_b32 s12, s16, 0
	s_cmp_gt_u32 s13, 61
	s_mov_b32 s16, s13
	s_waitcnt vmcnt(7)
	v_cvt_pk_bf16_f32 v20, v20, v38
	v_cvt_pk_bf16_f32 v21, v21, v39
	v_cvt_pk_bf16_f32 v22, v22, v40
	v_cvt_pk_bf16_f32 v23, v23, v41
	ds_write_b128 v19, v[20:23]
	s_cbranch_scc0 .LBB0_3337
	s_waitcnt vmcnt(0)
	s_mov_b64 s[16:17], 0

.LBB0_3344:
	s_add_i32 s13, s14, 2
	s_add_i32 s14, s14, 4
	s_min_u32 s14, s14, 63
	s_mul_i32 s15, s12, 0xa000
	s_lshl_b32 s64, s14, 6
	s_add_i32 s16, s15, 0xffff6000
	s_cmp_lg_u32 s12, 0
	s_cselect_b32 s16, s16, 0x14000
	s_add_i32 s16, s18, s16
	s_waitcnt lgkmcnt(0)
	s_barrier
	v_lshl_add_u64 v[188:189], v[202:203], 0, s[64:65]
	s_mov_b32 m0, s16
	s_nop 0
	global_load_lds_dwordx4 v[188:189], off
	v_lshl_add_u64 v[188:189], v[204:205], 0, s[64:65]
	s_add_i32 m0, s16, 0x400
	s_nop 0
	global_load_lds_dwordx4 v[188:189], off
	v_lshl_add_u64 v[188:189], v[206:207], 0, s[64:65]
	s_add_i32 m0, s16, 0x800
	s_nop 0
	global_load_lds_dwordx4 v[188:189], off
	v_lshl_add_u64 v[188:189], v[208:209], 0, s[64:65]
	s_add_i32 m0, s16, 0xc00
	s_nop 0
	global_load_lds_dwordx4 v[188:189], off
	v_lshl_add_u64 v[188:189], v[210:211], 0, s[64:65]
	s_add_i32 m0, s16, 0x1000
	s_lshl_b32 s64, s14, 16
	global_load_lds_dwordx4 v[188:189], off
	v_lshl_add_u64 v[192:193], v[212:213], 0, s[64:65]
	global_load_dwordx4 v[188:191], v[192:193], off nt
	s_nop 0
	global_load_dwordx4 v[192:195], v[192:193], off offset:2048 nt
	v_add_u32_e32 v216, s15, v86
	ds_read2_b32 v[196:197], v201 offset0:0 offset1:0x84
	ds_read2_b32 v[198:199], v232 offset0:0 offset1:0x84
	ds_read2_b32 v[222:223], v201 offset0:16 offset1:0x94
	ds_read2_b32 v[224:225], v232 offset0:16 offset1:0x94
	ds_read2_b32 v[226:227], v201 offset0:32 offset1:0xa4
	ds_read2_b32 v[228:229], v232 offset0:32 offset1:0xa4
	ds_read2_b32 v[238:239], v201 offset0:48 offset1:0xb4
	ds_read2_b32 v[240:241], v232 offset0:48 offset1:0xb4
	ds_read_b128 v[242:245], v216 offset:0
	ds_read_b128 v[246:249], v216 offset:0x400
	s_nop 0
	s_waitcnt lgkmcnt(1)
	s_setprio 1
	v_mfma_f32_16x16x32_bf16 v[140:143], v[196:199], v[242:245], v[140:143]
	v_mfma_f32_16x16x32_bf16 v[132:135], v[222:225], v[242:245], v[132:135]
	v_mfma_f32_16x16x32_bf16 v[144:147], v[226:229], v[242:245], v[144:147]
	v_mfma_f32_16x16x32_bf16 v[136:139], v[238:241], v[242:245], v[136:139]
	ds_read_b128 v[242:245], v216 offset:0x800
	s_waitcnt lgkmcnt(1)
	s_nop 0
	v_mfma_f32_16x16x32_bf16 v[124:127], v[196:199], v[246:249], v[124:127]
	v_mfma_f32_16x16x32_bf16 v[112:115], v[222:225], v[246:249], v[112:115]
	v_mfma_f32_16x16x32_bf16 v[128:131], v[226:229], v[246:249], v[128:131]
	v_mfma_f32_16x16x32_bf16 v[116:119], v[238:241], v[246:249], v[116:119]
	ds_read_b128 v[246:249], v216 offset:0xc00
	s_waitcnt lgkmcnt(1)
	s_nop 0
	v_mfma_f32_16x16x32_bf16 v[82:85], v[196:199], v[242:245], v[82:85]
	v_mfma_f32_16x16x32_bf16 v[54:57], v[222:225], v[242:245], v[54:57]
	v_mfma_f32_16x16x32_bf16 v[88:91], v[226:229], v[242:245], v[88:91]
	v_mfma_f32_16x16x32_bf16 v[58:61], v[238:241], v[242:245], v[58:61]
	ds_read_b128 v[242:245], v216 offset:0x1000
	s_waitcnt lgkmcnt(1)
	s_nop 0
	v_mfma_f32_16x16x32_bf16 v[26:29], v[196:199], v[246:249], v[26:29]
	v_mfma_f32_16x16x32_bf16 v[6:9], v[222:225], v[246:249], v[6:9]
	v_mfma_f32_16x16x32_bf16 v[42:45], v[226:229], v[246:249], v[42:45]
	v_mfma_f32_16x16x32_bf16 v[14:17], v[238:241], v[246:249], v[14:17]
	ds_read_b128 v[246:249], v216 offset:0x1400
	s_waitcnt lgkmcnt(1)
	s_nop 0
	v_mfma_f32_16x16x32_bf16 v[92:95], v[196:199], v[242:245], v[92:95]
	v_mfma_f32_16x16x32_bf16 v[62:65], v[222:225], v[242:245], v[62:65]
	v_mfma_f32_16x16x32_bf16 v[96:99], v[226:229], v[242:245], v[96:99]
	v_mfma_f32_16x16x32_bf16 v[66:69], v[238:241], v[242:245], v[66:69]
	ds_read_b128 v[242:245], v216 offset:0x1800
	s_waitcnt lgkmcnt(1)
	s_nop 0
	v_mfma_f32_16x16x32_bf16 v[38:41], v[196:199], v[246:249], v[38:41]
	v_mfma_f32_16x16x32_bf16 v[18:21], v[222:225], v[246:249], v[18:21]
	v_mfma_f32_16x16x32_bf16 v[46:49], v[226:229], v[246:249], v[46:49]
	v_mfma_f32_16x16x32_bf16 v[22:25], v[238:241], v[246:249], v[22:25]
	ds_read_b128 v[246:249], v216 offset:0x1c00
	s_waitcnt lgkmcnt(1)
	s_nop 0
	v_mfma_f32_16x16x32_bf16 v[108:111], v[196:199], v[242:245], v[108:111]
	v_mfma_f32_16x16x32_bf16 v[100:103], v[222:225], v[242:245], v[100:103]
	v_mfma_f32_16x16x32_bf16 v[120:123], v[226:229], v[242:245], v[120:123]
	v_mfma_f32_16x16x32_bf16 v[104:107], v[238:241], v[242:245], v[104:107]
	ds_read_b128 v[242:245], v216 offset:0x2000
	s_waitcnt lgkmcnt(1)
	s_nop 0
	v_mfma_f32_16x16x32_bf16 v[70:73], v[196:199], v[246:249], v[70:73]
	v_mfma_f32_16x16x32_bf16 v[50:53], v[222:225], v[246:249], v[50:53]
	v_mfma_f32_16x16x32_bf16 v[10:13], v[226:229], v[246:249], v[10:13]
	v_mfma_f32_16x16x32_bf16 v[2:5], v[238:241], v[246:249], v[2:5]
	ds_read_b128 v[246:249], v216 offset:0x2400
	s_waitcnt lgkmcnt(1)
	s_nop 0
	v_mfma_f32_16x16x32_bf16 v[176:179], v[196:199], v[242:245], v[176:179]
	s_waitcnt lgkmcnt(0)
	v_mfma_f32_16x16x32_bf16 v[168:171], v[222:225], v[242:245], v[168:171]
	v_mfma_f32_16x16x32_bf16 v[172:175], v[226:229], v[242:245], v[172:175]
	v_mfma_f32_16x16x32_bf16 v[164:167], v[238:241], v[242:245], v[164:167]
	v_mfma_f32_16x16x32_bf16 v[160:163], v[196:199], v[246:249], v[160:163]
	v_mfma_f32_16x16x32_bf16 v[152:155], v[222:225], v[246:249], v[152:155]
	v_mfma_f32_16x16x32_bf16 v[156:159], v[226:229], v[246:249], v[156:159]
	v_mfma_f32_16x16x32_bf16 v[148:151], v[238:241], v[246:249], v[148:151]
	s_setprio 0
	s_add_i32 s14, s12, 1
	s_cmp_lg_u32 s12, 2
	s_cselect_b32 s12, s14, 0
	s_min_u32 s14, s13, 60
	s_add_i32 s14, s14, 3
	s_mul_i32 s15, s12, 0xa000
	s_lshl_b32 s64, s14, 6
	s_add_i32 s16, s15, 0xffff6000
	s_cmp_lg_u32 s12, 0
	s_waitcnt vmcnt(7)
	v_cvt_pk_bf16_f32 v180, v184, v180
	v_add_u32_e32 v184, 0x20100, v235
	s_cselect_b32 s16, s16, 0x14000
	v_cvt_pk_bf16_f32 v181, v185, v181
	v_cvt_pk_bf16_f32 v182, v186, v182
	v_cvt_pk_bf16_f32 v183, v187, v183
	ds_write_b128 v184, v[180:183]
	v_lshl_add_u64 v[196:197], v[202:203], 0, s[64:65]
	v_lshl_add_u64 v[198:199], v[204:205], 0, s[64:65]
	v_lshl_add_u64 v[216:217], v[206:207], 0, s[64:65]
	v_lshl_add_u64 v[222:223], v[208:209], 0, s[64:65]
	v_lshl_add_u64 v[224:225], v[210:211], 0, s[64:65]
	s_lshl_b32 s64, s14, 16
	s_add_i32 s14, s18, s16
	s_waitcnt lgkmcnt(0)
	s_barrier
	v_lshl_add_u64 v[180:181], v[212:213], 0, s[64:65]
	s_mov_b32 m0, s14
	global_load_dwordx4 v[184:187], v[180:181], off nt
	s_nop 0
	global_load_dwordx4 v[180:183], v[180:181], off offset:2048 nt
	s_nop 0
	global_load_lds_dwordx4 v[196:197], off
	s_add_i32 m0, s14, 0x400
	s_nop 0
	global_load_lds_dwordx4 v[198:199], off
	s_add_i32 m0, s14, 0x800
	s_nop 0
	global_load_lds_dwordx4 v[216:217], off
	s_add_i32 m0, s14, 0xc00
	s_nop 0
	global_load_lds_dwordx4 v[222:223], off
	s_add_i32 m0, s14, 0x1000
	s_nop 0
	global_load_lds_dwordx4 v[224:225], off
	v_add_u32_e32 v216, s15, v86
	ds_read2_b32 v[196:197], v233 offset0:0 offset1:0x84
	ds_read2_b32 v[198:199], v234 offset0:0 offset1:0x84
	ds_read2_b32 v[222:223], v233 offset0:16 offset1:0x94
	ds_read2_b32 v[224:225], v234 offset0:16 offset1:0x94
	ds_read2_b32 v[226:227], v233 offset0:32 offset1:0xa4
	ds_read2_b32 v[228:229], v234 offset0:32 offset1:0xa4
	ds_read2_b32 v[238:239], v233 offset0:48 offset1:0xb4
	ds_read2_b32 v[240:241], v234 offset0:48 offset1:0xb4
	ds_read_b128 v[242:245], v216 offset:0
	ds_read_b128 v[246:249], v216 offset:0x400
	s_nop 0
	s_waitcnt lgkmcnt(1)
	s_setprio 1
	v_mfma_f32_16x16x32_bf16 v[140:143], v[196:199], v[242:245], v[140:143]
	v_mfma_f32_16x16x32_bf16 v[132:135], v[222:225], v[242:245], v[132:135]
	v_mfma_f32_16x16x32_bf16 v[144:147], v[226:229], v[242:245], v[144:147]
	v_mfma_f32_16x16x32_bf16 v[136:139], v[238:241], v[242:245], v[136:139]
	ds_read_b128 v[242:245], v216 offset:0x800
	s_waitcnt lgkmcnt(1)
	s_nop 0
	v_mfma_f32_16x16x32_bf16 v[124:127], v[196:199], v[246:249], v[124:127]
	v_mfma_f32_16x16x32_bf16 v[112:115], v[222:225], v[246:249], v[112:115]
	v_mfma_f32_16x16x32_bf16 v[128:131], v[226:229], v[246:249], v[128:131]
	v_mfma_f32_16x16x32_bf16 v[116:119], v[238:241], v[246:249], v[116:119]
	ds_read_b128 v[246:249], v216 offset:0xc00
	s_waitcnt lgkmcnt(1)
	s_nop 0
	v_mfma_f32_16x16x32_bf16 v[82:85], v[196:199], v[242:245], v[82:85]
	v_mfma_f32_16x16x32_bf16 v[54:57], v[222:225], v[242:245], v[54:57]
	v_mfma_f32_16x16x32_bf16 v[88:91], v[226:229], v[242:245], v[88:91]
	v_mfma_f32_16x16x32_bf16 v[58:61], v[238:241], v[242:245], v[58:61]
	ds_read_b128 v[242:245], v216 offset:0x1000
	s_waitcnt lgkmcnt(1)
	s_nop 0
	v_mfma_f32_16x16x32_bf16 v[26:29], v[196:199], v[246:249], v[26:29]
	v_mfma_f32_16x16x32_bf16 v[6:9], v[222:225], v[246:249], v[6:9]
	v_mfma_f32_16x16x32_bf16 v[42:45], v[226:229], v[246:249], v[42:45]
	v_mfma_f32_16x16x32_bf16 v[14:17], v[238:241], v[246:249], v[14:17]
	ds_read_b128 v[246:249], v216 offset:0x1400
	s_waitcnt lgkmcnt(1)
	s_nop 0
	v_mfma_f32_16x16x32_bf16 v[92:95], v[196:199], v[242:245], v[92:95]
	v_mfma_f32_16x16x32_bf16 v[62:65], v[222:225], v[242:245], v[62:65]
	v_mfma_f32_16x16x32_bf16 v[96:99], v[226:229], v[242:245], v[96:99]
	v_mfma_f32_16x16x32_bf16 v[66:69], v[238:241], v[242:245], v[66:69]
	ds_read_b128 v[242:245], v216 offset:0x1800
	s_waitcnt lgkmcnt(1)
	s_nop 0
	v_mfma_f32_16x16x32_bf16 v[38:41], v[196:199], v[246:249], v[38:41]
	v_mfma_f32_16x16x32_bf16 v[18:21], v[222:225], v[246:249], v[18:21]
	v_mfma_f32_16x16x32_bf16 v[46:49], v[226:229], v[246:249], v[46:49]
	v_mfma_f32_16x16x32_bf16 v[22:25], v[238:241], v[246:249], v[22:25]
	ds_read_b128 v[246:249], v216 offset:0x1c00
	s_waitcnt lgkmcnt(1)
	s_nop 0
	v_mfma_f32_16x16x32_bf16 v[108:111], v[196:199], v[242:245], v[108:111]
	v_mfma_f32_16x16x32_bf16 v[100:103], v[222:225], v[242:245], v[100:103]
	v_mfma_f32_16x16x32_bf16 v[120:123], v[226:229], v[242:245], v[120:123]
	v_mfma_f32_16x16x32_bf16 v[104:107], v[238:241], v[242:245], v[104:107]
	ds_read_b128 v[242:245], v216 offset:0x2000
	s_waitcnt lgkmcnt(1)
	s_nop 0
	v_mfma_f32_16x16x32_bf16 v[70:73], v[196:199], v[246:249], v[70:73]
	v_mfma_f32_16x16x32_bf16 v[50:53], v[222:225], v[246:249], v[50:53]
	v_mfma_f32_16x16x32_bf16 v[10:13], v[226:229], v[246:249], v[10:13]
	v_mfma_f32_16x16x32_bf16 v[2:5], v[238:241], v[246:249], v[2:5]
	ds_read_b128 v[246:249], v216 offset:0x2400
	s_waitcnt lgkmcnt(1)
	s_nop 0
	v_mfma_f32_16x16x32_bf16 v[176:179], v[196:199], v[242:245], v[176:179]
	s_waitcnt lgkmcnt(0)
	v_mfma_f32_16x16x32_bf16 v[168:171], v[222:225], v[242:245], v[168:171]
	v_mfma_f32_16x16x32_bf16 v[172:175], v[226:229], v[242:245], v[172:175]
	v_mfma_f32_16x16x32_bf16 v[164:167], v[238:241], v[242:245], v[164:167]
	v_mfma_f32_16x16x32_bf16 v[160:163], v[196:199], v[246:249], v[160:163]
	v_mfma_f32_16x16x32_bf16 v[152:155], v[222:225], v[246:249], v[152:155]
	v_mfma_f32_16x16x32_bf16 v[156:159], v[226:229], v[246:249], v[156:159]
	v_mfma_f32_16x16x32_bf16 v[148:151], v[238:241], v[246:249], v[148:151]
	s_setprio 0
	s_waitcnt vmcnt(7)
	s_add_i32 s14, s12, 1
	s_cmp_lg_u32 s12, 2
	s_cselect_b32 s12, s14, 0
	s_cmp_gt_u32 s13, 61
	s_mov_b32 s14, s13
	s_waitcnt vmcnt(7)
	v_cvt_pk_bf16_f32 v188, v188, v192
	v_cvt_pk_bf16_f32 v189, v189, v193
	v_cvt_pk_bf16_f32 v190, v190, v194
	v_cvt_pk_bf16_f32 v191, v191, v195
	ds_write_b128 v236, v[188:191]
	s_cbranch_scc0 .LBB0_3344
	s_waitcnt vmcnt(0)
	s_mov_b64 s[12:13], 0

.LBB0_3348:
	s_add_i32 s12, s14, 2
	s_add_i32 s14, s14, 4
	s_min_u32 s14, s14, 63
	s_mul_i32 s15, s13, 0xa000
	s_lshl_b32 s64, s14, 6
	s_add_i32 s16, s15, 0xffff6000
	s_cmp_lg_u32 s13, 0
	s_cselect_b32 s16, s16, 0x14000
	s_add_i32 s16, s18, s16
	s_waitcnt lgkmcnt(0)
	s_barrier
	v_lshl_add_u64 v[2:3], v[202:203], 0, s[64:65]
	s_mov_b32 m0, s16
	s_nop 0
	global_load_lds_dwordx4 v[2:3], off
	v_lshl_add_u64 v[2:3], v[204:205], 0, s[64:65]
	s_add_i32 m0, s16, 0x400
	s_nop 0
	global_load_lds_dwordx4 v[2:3], off
	v_lshl_add_u64 v[2:3], v[206:207], 0, s[64:65]
	s_add_i32 m0, s16, 0x800
	s_nop 0
	global_load_lds_dwordx4 v[2:3], off
	v_lshl_add_u64 v[2:3], v[208:209], 0, s[64:65]
	s_add_i32 m0, s16, 0xc00
	s_nop 0
	global_load_lds_dwordx4 v[2:3], off
	v_lshl_add_u64 v[2:3], v[210:211], 0, s[64:65]
	s_add_i32 m0, s16, 0x1000
	s_lshl_b32 s64, s14, 16
	global_load_lds_dwordx4 v[2:3], off
	v_lshl_add_u64 v[6:7], v[212:213], 0, s[64:65]
	global_load_dwordx4 v[2:5], v[6:7], off nt
	s_nop 0
	global_load_dwordx4 v[6:9], v[6:7], off offset:2048 nt
	v_add_u32_e32 v38, s15, v86
	ds_read2_b32 v[10:11], v201 offset0:0 offset1:0x84
	ds_read2_b32 v[12:13], v232 offset0:0 offset1:0x84
	ds_read2_b32 v[14:15], v201 offset0:16 offset1:0x94
	ds_read2_b32 v[16:17], v232 offset0:16 offset1:0x94
	ds_read2_b32 v[18:19], v201 offset0:32 offset1:0xa4
	ds_read2_b32 v[20:21], v232 offset0:32 offset1:0xa4
	ds_read2_b32 v[22:23], v201 offset0:48 offset1:0xb4
	ds_read2_b32 v[24:25], v232 offset0:48 offset1:0xb4
	ds_read_b128 v[26:29], v38 offset:0
	ds_read_b128 v[38:41], v38 offset:0x400
	s_nop 0
	s_waitcnt lgkmcnt(1)
	s_setprio 1
	v_mfma_f32_16x16x32_bf16 v[42:45], v[10:13], v[26:29], v[140:143]
	s_waitcnt lgkmcnt(0)
	v_mfma_f32_16x16x32_bf16 v[46:49], v[14:17], v[26:29], v[132:135]
	v_mfma_f32_16x16x32_bf16 v[50:53], v[18:21], v[26:29], v[144:147]
	v_mfma_f32_16x16x32_bf16 v[26:29], v[22:25], v[26:29], v[136:139]
	v_mfma_f32_16x16x32_bf16 v[10:13], v[10:13], v[38:41], v[124:127]
	v_mfma_f32_16x16x32_bf16 v[14:17], v[14:17], v[38:41], v[112:115]
	v_mfma_f32_16x16x32_bf16 v[18:21], v[18:21], v[38:41], v[128:131]
	v_mfma_f32_16x16x32_bf16 v[22:25], v[22:25], v[38:41], v[116:119]
	s_setprio 0
	s_add_i32 s14, s13, 1
	s_cmp_lg_u32 s13, 2
	s_cselect_b32 s13, s14, 0
	s_min_u32 s14, s12, 60
	s_add_i32 s14, s14, 3
	s_mul_i32 s15, s13, 0xa000
	s_lshl_b32 s64, s14, 6
	s_add_i32 s16, s15, 0xffff6000
	s_cmp_lg_u32 s13, 0
	s_waitcnt vmcnt(7)
	v_cvt_pk_bf16_f32 v30, v30, v34
	v_add_u32_e32 v34, 0x20100, v235
	s_cselect_b32 s16, s16, 0x14000
	v_cvt_pk_bf16_f32 v31, v31, v35
	v_cvt_pk_bf16_f32 v32, v32, v36
	v_cvt_pk_bf16_f32 v33, v33, v37
	ds_write_b128 v34, v[30:33]
	v_lshl_add_u64 v[38:39], v[202:203], 0, s[64:65]
	v_lshl_add_u64 v[40:41], v[204:205], 0, s[64:65]
	v_lshl_add_u64 v[54:55], v[206:207], 0, s[64:65]
	v_lshl_add_u64 v[56:57], v[208:209], 0, s[64:65]
	v_lshl_add_u64 v[58:59], v[210:211], 0, s[64:65]
	s_lshl_b32 s64, s14, 16
	s_add_i32 s14, s18, s16
	s_waitcnt lgkmcnt(0)
	s_barrier
	v_lshl_add_u64 v[34:35], v[212:213], 0, s[64:65]
	s_mov_b32 m0, s14
	global_load_dwordx4 v[30:33], v[34:35], off nt
	s_nop 0
	global_load_dwordx4 v[34:37], v[34:35], off offset:2048 nt
	s_nop 0
	global_load_lds_dwordx4 v[38:39], off
	s_add_i32 m0, s14, 0x400
	s_nop 0
	global_load_lds_dwordx4 v[40:41], off
	s_add_i32 m0, s14, 0x800
	s_nop 0
	global_load_lds_dwordx4 v[54:55], off
	s_add_i32 m0, s14, 0xc00
	s_nop 0
	global_load_lds_dwordx4 v[56:57], off
	s_add_i32 m0, s14, 0x1000
	s_nop 0
	global_load_lds_dwordx4 v[58:59], off
	v_add_u32_e32 v70, s15, v86
	ds_read2_b32 v[38:39], v233 offset0:0 offset1:0x84
	ds_read2_b32 v[40:41], v234 offset0:0 offset1:0x84
	ds_read2_b32 v[54:55], v233 offset0:16 offset1:0x94
	ds_read2_b32 v[56:57], v234 offset0:16 offset1:0x94
	ds_read2_b32 v[58:59], v233 offset0:32 offset1:0xa4
	ds_read2_b32 v[60:61], v234 offset0:32 offset1:0xa4
	ds_read2_b32 v[62:63], v233 offset0:48 offset1:0xb4
	ds_read2_b32 v[64:65], v234 offset0:48 offset1:0xb4
	ds_read_b128 v[66:69], v70 offset:0
	ds_read_b128 v[70:73], v70 offset:0x400
	s_nop 0
	s_waitcnt lgkmcnt(1)
	s_setprio 1
	v_mfma_f32_16x16x32_bf16 v[140:143], v[38:41], v[66:69], v[42:45]
	s_waitcnt lgkmcnt(0)
	v_mfma_f32_16x16x32_bf16 v[132:135], v[54:57], v[66:69], v[46:49]
	v_mfma_f32_16x16x32_bf16 v[144:147], v[58:61], v[66:69], v[50:53]
	v_mfma_f32_16x16x32_bf16 v[136:139], v[62:65], v[66:69], v[26:29]
	v_mfma_f32_16x16x32_bf16 v[124:127], v[38:41], v[70:73], v[10:13]
	v_mfma_f32_16x16x32_bf16 v[112:115], v[54:57], v[70:73], v[14:17]
	v_mfma_f32_16x16x32_bf16 v[128:131], v[58:61], v[70:73], v[18:21]
	v_mfma_f32_16x16x32_bf16 v[116:119], v[62:65], v[70:73], v[22:25]
	s_setprio 0
	s_waitcnt vmcnt(7)
	s_add_i32 s14, s13, 1
	s_cmp_lg_u32 s13, 2
	s_cselect_b32 s13, s14, 0
	s_cmp_gt_u32 s12, 61
	s_mov_b32 s14, s12
	s_waitcnt vmcnt(7)
	v_cvt_pk_bf16_f32 v2, v2, v6
	v_cvt_pk_bf16_f32 v3, v3, v7
	v_cvt_pk_bf16_f32 v4, v4, v8
	v_cvt_pk_bf16_f32 v5, v5, v9
	ds_write_b128 v236, v[2:5]
	s_cbranch_scc0 .LBB0_3348
	s_waitcnt vmcnt(0)
	v_mov_b32_e32 v151, 0
	v_mov_b32_e32 v150, v151
	v_mov_b32_e32 v149, v151
	v_mov_b32_e32 v148, v151
	v_mov_b32_e32 v159, v151
	v_mov_b32_e32 v158, v151
	v_mov_b32_e32 v157, v151
	v_mov_b32_e32 v156, v151
	v_mov_b32_e32 v155, v151
	v_mov_b32_e32 v154, v151
	v_mov_b32_e32 v153, v151
	v_mov_b32_e32 v152, v151
	v_mov_b32_e32 v163, v151
	v_mov_b32_e32 v162, v151
	v_mov_b32_e32 v161, v151
	v_mov_b32_e32 v160, v151
	v_mov_b32_e32 v167, v151
	v_mov_b32_e32 v166, v151
	v_mov_b32_e32 v165, v151
	v_mov_b32_e32 v164, v151
	v_mov_b32_e32 v175, v151
	v_mov_b32_e32 v174, v151
	v_mov_b32_e32 v173, v151
	v_mov_b32_e32 v172, v151
	v_mov_b32_e32 v171, v151
	v_mov_b32_e32 v170, v151
	v_mov_b32_e32 v169, v151
	v_mov_b32_e32 v168, v151
	v_mov_b32_e32 v179, v151
	v_mov_b32_e32 v178, v151
	v_mov_b32_e32 v177, v151
	v_mov_b32_e32 v176, v151
	v_mov_b32_e32 v5, v151
	v_mov_b32_e32 v4, v151
	v_mov_b32_e32 v3, v151
	v_mov_b32_e32 v2, v151
	v_mov_b32_e32 v13, v151
	v_mov_b32_e32 v12, v151
	v_mov_b32_e32 v11, v151
	v_mov_b32_e32 v10, v151
	v_mov_b32_e32 v85, v151
	v_mov_b32_e32 v84, v151
	v_mov_b32_e32 v83, v151
	v_mov_b32_e32 v82, v151
	v_mov_b32_e32 v57, v151
	v_mov_b32_e32 v56, v151
	v_mov_b32_e32 v55, v151
	v_mov_b32_e32 v54, v151
	v_mov_b32_e32 v91, v151
	v_mov_b32_e32 v90, v151
	v_mov_b32_e32 v89, v151
	v_mov_b32_e32 v88, v151
	v_mov_b32_e32 v61, v151
	v_mov_b32_e32 v60, v151
	v_mov_b32_e32 v59, v151
	v_mov_b32_e32 v58, v151
	v_mov_b32_e32 v29, v151
	v_mov_b32_e32 v28, v151
	v_mov_b32_e32 v27, v151
	v_mov_b32_e32 v26, v151
	v_mov_b32_e32 v9, v151
	v_mov_b32_e32 v8, v151
	v_mov_b32_e32 v7, v151
	v_mov_b32_e32 v6, v151
	v_mov_b32_e32 v45, v151
	v_mov_b32_e32 v44, v151
	v_mov_b32_e32 v43, v151
	v_mov_b32_e32 v42, v151
	v_mov_b32_e32 v17, v151
	v_mov_b32_e32 v16, v151
	v_mov_b32_e32 v15, v151
	v_mov_b32_e32 v14, v151
	v_mov_b32_e32 v95, v151
	v_mov_b32_e32 v94, v151
	v_mov_b32_e32 v93, v151
	v_mov_b32_e32 v92, v151
	v_mov_b32_e32 v65, v151
	v_mov_b32_e32 v64, v151
	v_mov_b32_e32 v63, v151
	v_mov_b32_e32 v62, v151
	v_mov_b32_e32 v99, v151
	v_mov_b32_e32 v98, v151
	v_mov_b32_e32 v97, v151
	v_mov_b32_e32 v96, v151
	v_mov_b32_e32 v69, v151
	v_mov_b32_e32 v68, v151
	v_mov_b32_e32 v67, v151
	v_mov_b32_e32 v66, v151
	v_mov_b32_e32 v41, v151
	v_mov_b32_e32 v40, v151
	v_mov_b32_e32 v39, v151
	v_mov_b32_e32 v38, v151
	v_mov_b32_e32 v21, v151
	v_mov_b32_e32 v20, v151
	v_mov_b32_e32 v19, v151
	v_mov_b32_e32 v18, v151
	v_mov_b32_e32 v49, v151
	v_mov_b32_e32 v48, v151
	v_mov_b32_e32 v47, v151
	v_mov_b32_e32 v46, v151
	v_mov_b32_e32 v25, v151
	v_mov_b32_e32 v24, v151
	v_mov_b32_e32 v23, v151
	v_mov_b32_e32 v22, v151
	v_mov_b32_e32 v111, v151
	v_mov_b32_e32 v110, v151
	v_mov_b32_e32 v109, v151
	v_mov_b32_e32 v108, v151
	v_mov_b32_e32 v103, v151
	v_mov_b32_e32 v102, v151
	v_mov_b32_e32 v101, v151
	v_mov_b32_e32 v100, v151
	v_mov_b32_e32 v123, v151
	v_mov_b32_e32 v122, v151
	v_mov_b32_e32 v121, v151
	v_mov_b32_e32 v120, v151
	v_mov_b32_e32 v107, v151
	v_mov_b32_e32 v106, v151
	v_mov_b32_e32 v105, v151
	v_mov_b32_e32 v104, v151
	v_mov_b32_e32 v73, v151
	v_mov_b32_e32 v72, v151
	v_mov_b32_e32 v71, v151
	v_mov_b32_e32 v70, v151
	v_mov_b32_e32 v53, v151
	v_mov_b32_e32 v52, v151
	v_mov_b32_e32 v51, v151
	v_mov_b32_e32 v50, v151

.LBB0_3448:
	s_add_i32 s7, s8, 2
	s_add_i32 s8, s8, 4
	s_min_u32 s8, s8, 15
	s_mul_i32 s9, s6, 0xa000
	s_lshl_b32 s64, s8, 6
	s_add_i32 s24, s9, 0xffff6000
	s_cmp_lg_u32 s6, 0
	s_cselect_b32 s24, s24, 0x14000
	s_add_i32 s24, s22, s24
	s_waitcnt lgkmcnt(0)
	s_barrier
	v_lshl_add_u64 v[156:157], v[200:201], 0, s[64:65]
	s_mov_b32 m0, s24
	s_nop 0
	global_load_lds_dwordx4 v[156:157], off
	v_lshl_add_u64 v[156:157], v[202:203], 0, s[64:65]
	s_add_i32 m0, s24, 0x400
	s_nop 0
	global_load_lds_dwordx4 v[156:157], off
	v_lshl_add_u64 v[156:157], v[204:205], 0, s[64:65]
	s_add_i32 m0, s24, 0x800
	s_nop 0
	global_load_lds_dwordx4 v[156:157], off
	v_lshl_add_u64 v[156:157], v[206:207], 0, s[64:65]
	s_add_i32 m0, s24, 0xc00
	s_nop 0
	global_load_lds_dwordx4 v[156:157], off
	v_lshl_add_u64 v[156:157], v[208:209], 0, s[64:65]
	s_add_i32 m0, s24, 0x1000
	s_lshl_b32 s64, s8, 18
	global_load_lds_dwordx4 v[156:157], off
	v_lshl_add_u64 v[156:157], v[210:211], 0, s[64:65]
	v_add_co_u32_e32 v160, vcc, s33, v156
	s_nop 1
	v_addc_co_u32_e32 v161, vcc, 0, v157, vcc
	global_load_dwordx4 v[156:159], v[156:157], off nt
	s_nop 0
	global_load_dwordx4 v[160:163], v[160:161], off nt
	v_add_u32_e32 v167, s9, v86
	ds_read2_b32 v[168:169], v232 offset0:0 offset1:0x84
	ds_read2_b32 v[170:171], v233 offset0:0 offset1:0x84
	ds_read2_b32 v[172:173], v232 offset0:16 offset1:0x94
	ds_read2_b32 v[174:175], v233 offset0:16 offset1:0x94
	ds_read2_b32 v[176:177], v232 offset0:32 offset1:0xa4
	ds_read2_b32 v[178:179], v233 offset0:32 offset1:0xa4
	ds_read2_b32 v[180:181], v232 offset0:48 offset1:0xb4
	ds_read2_b32 v[182:183], v233 offset0:48 offset1:0xb4
	ds_read_b128 v[184:187], v167 offset:0
	ds_read_b128 v[188:191], v167 offset:0x400
	s_nop 0
	s_waitcnt lgkmcnt(1)
	s_setprio 1
	v_mfma_f32_16x16x32_bf16 v[78:81], v[168:171], v[184:187], v[78:81]
	v_mfma_f32_16x16x32_bf16 v[74:77], v[172:175], v[184:187], v[74:77]
	v_mfma_f32_16x16x32_bf16 v[70:73], v[176:179], v[184:187], v[70:73]
	v_mfma_f32_16x16x32_bf16 v[66:69], v[180:183], v[184:187], v[66:69]
	ds_read_b128 v[184:187], v167 offset:0x800
	s_waitcnt lgkmcnt(1)
	s_nop 0
	v_mfma_f32_16x16x32_bf16 v[62:65], v[168:171], v[188:191], v[62:65]
	v_mfma_f32_16x16x32_bf16 v[58:61], v[172:175], v[188:191], v[58:61]
	v_mfma_f32_16x16x32_bf16 v[54:57], v[176:179], v[188:191], v[54:57]
	v_mfma_f32_16x16x32_bf16 v[50:53], v[180:183], v[188:191], v[50:53]
	ds_read_b128 v[188:191], v167 offset:0xc00
	s_waitcnt lgkmcnt(1)
	s_nop 0
	v_mfma_f32_16x16x32_bf16 v[46:49], v[168:171], v[184:187], v[46:49]
	v_mfma_f32_16x16x32_bf16 v[42:45], v[172:175], v[184:187], v[42:45]
	v_mfma_f32_16x16x32_bf16 v[38:41], v[176:179], v[184:187], v[38:41]
	v_mfma_f32_16x16x32_bf16 v[34:37], v[180:183], v[184:187], v[34:37]
	ds_read_b128 v[184:187], v167 offset:0x1000
	s_waitcnt lgkmcnt(1)
	s_nop 0
	v_mfma_f32_16x16x32_bf16 v[18:21], v[168:171], v[188:191], v[18:21]
	v_mfma_f32_16x16x32_bf16 v[22:25], v[172:175], v[188:191], v[22:25]
	v_mfma_f32_16x16x32_bf16 v[26:29], v[176:179], v[188:191], v[26:29]
	v_mfma_f32_16x16x32_bf16 v[30:33], v[180:183], v[188:191], v[30:33]
	ds_read_b128 v[188:191], v167 offset:0x1400
	s_waitcnt lgkmcnt(1)
	s_nop 0
	v_mfma_f32_16x16x32_bf16 v[88:91], v[168:171], v[184:187], v[88:91]
	v_mfma_f32_16x16x32_bf16 v[112:115], v[172:175], v[184:187], v[112:115]
	v_mfma_f32_16x16x32_bf16 v[108:111], v[176:179], v[184:187], v[108:111]
	v_mfma_f32_16x16x32_bf16 v[100:103], v[180:183], v[184:187], v[100:103]
	ds_read_b128 v[184:187], v167 offset:0x1800
	s_waitcnt lgkmcnt(1)
	s_nop 0
	v_mfma_f32_16x16x32_bf16 v[82:85], v[168:171], v[188:191], v[82:85]
	v_mfma_f32_16x16x32_bf16 v[92:95], v[172:175], v[188:191], v[92:95]
	v_mfma_f32_16x16x32_bf16 v[96:99], v[176:179], v[188:191], v[96:99]
	v_mfma_f32_16x16x32_bf16 v[104:107], v[180:183], v[188:191], v[104:107]
	ds_read_b128 v[188:191], v167 offset:0x1c00
	s_waitcnt lgkmcnt(1)
	s_nop 0
	v_mfma_f32_16x16x32_bf16 v[116:119], v[168:171], v[184:187], v[116:119]
	s_waitcnt lgkmcnt(0)
	v_mfma_f32_16x16x32_bf16 v[124:127], v[172:175], v[184:187], v[124:127]
	v_mfma_f32_16x16x32_bf16 v[132:135], v[176:179], v[184:187], v[132:135]
	v_mfma_f32_16x16x32_bf16 v[136:139], v[180:183], v[184:187], v[136:139]
	v_mfma_f32_16x16x32_bf16 v[120:123], v[168:171], v[188:191], v[120:123]
	v_mfma_f32_16x16x32_bf16 v[128:131], v[172:175], v[188:191], v[128:131]
	v_mfma_f32_16x16x32_bf16 v[140:143], v[176:179], v[188:191], v[140:143]
	v_mfma_f32_16x16x32_bf16 v[144:147], v[180:183], v[188:191], v[144:147]
	s_setprio 0
	s_add_i32 s8, s6, 1
	s_cmp_lg_u32 s6, 2
	s_cselect_b32 s6, s8, 0
	s_min_u32 s8, s7, 12
	s_add_i32 s8, s8, 3
	s_mul_i32 s9, s6, 0xa000
	s_lshl_b32 s64, s8, 6
	s_add_i32 s24, s9, 0xffff6000
	s_cmp_lg_u32 s6, 0
	s_waitcnt vmcnt(7)
	v_cvt_pk_bf16_f32 v148, v148, v152
	v_add_u32_e32 v152, 0x20100, v165
	s_cselect_b32 s24, s24, 0x14000
	v_cvt_pk_bf16_f32 v149, v149, v153
	v_cvt_pk_bf16_f32 v150, v150, v154
	v_cvt_pk_bf16_f32 v151, v151, v155
	ds_write_b128 v152, v[148:151]
	s_add_i32 s24, s22, s24
	s_waitcnt lgkmcnt(0)
	s_barrier
	v_lshl_add_u64 v[148:149], v[200:201], 0, s[64:65]
	s_mov_b32 m0, s24
	s_nop 0
	global_load_lds_dwordx4 v[148:149], off
	v_lshl_add_u64 v[148:149], v[202:203], 0, s[64:65]
	s_add_i32 m0, s24, 0x400
	s_nop 0
	global_load_lds_dwordx4 v[148:149], off
	v_lshl_add_u64 v[148:149], v[204:205], 0, s[64:65]
	s_add_i32 m0, s24, 0x800
	s_nop 0
	global_load_lds_dwordx4 v[148:149], off
	v_lshl_add_u64 v[148:149], v[206:207], 0, s[64:65]
	s_add_i32 m0, s24, 0xc00
	s_nop 0
	global_load_lds_dwordx4 v[148:149], off
	v_lshl_add_u64 v[148:149], v[208:209], 0, s[64:65]
	s_lshl_b32 s64, s8, 18
	s_add_i32 m0, s24, 0x1000
	v_lshl_add_u64 v[152:153], v[210:211], 0, s[64:65]
	global_load_lds_dwordx4 v[148:149], off
	global_load_dwordx4 v[148:151], v[152:153], off nt
	v_add_co_u32_e32 v152, vcc, s33, v152
	s_nop 1
	v_addc_co_u32_e32 v153, vcc, 0, v153, vcc
	global_load_dwordx4 v[152:155], v[152:153], off nt
	v_add_u32_e32 v167, s9, v86
	ds_read2_b32 v[168:169], v234 offset0:0 offset1:0x84
	ds_read2_b32 v[170:171], v235 offset0:0 offset1:0x84
	ds_read2_b32 v[172:173], v234 offset0:16 offset1:0x94
	ds_read2_b32 v[174:175], v235 offset0:16 offset1:0x94
	ds_read2_b32 v[176:177], v234 offset0:32 offset1:0xa4
	ds_read2_b32 v[178:179], v235 offset0:32 offset1:0xa4
	ds_read2_b32 v[180:181], v234 offset0:48 offset1:0xb4
	ds_read2_b32 v[182:183], v235 offset0:48 offset1:0xb4
	ds_read_b128 v[184:187], v167 offset:0
	ds_read_b128 v[188:191], v167 offset:0x400
	s_nop 0
	s_waitcnt lgkmcnt(1)
	s_setprio 1
	v_mfma_f32_16x16x32_bf16 v[78:81], v[168:171], v[184:187], v[78:81]
	v_mfma_f32_16x16x32_bf16 v[74:77], v[172:175], v[184:187], v[74:77]
	v_mfma_f32_16x16x32_bf16 v[70:73], v[176:179], v[184:187], v[70:73]
	v_mfma_f32_16x16x32_bf16 v[66:69], v[180:183], v[184:187], v[66:69]
	ds_read_b128 v[184:187], v167 offset:0x800
	s_waitcnt lgkmcnt(1)
	s_nop 0
	v_mfma_f32_16x16x32_bf16 v[62:65], v[168:171], v[188:191], v[62:65]
	v_mfma_f32_16x16x32_bf16 v[58:61], v[172:175], v[188:191], v[58:61]
	v_mfma_f32_16x16x32_bf16 v[54:57], v[176:179], v[188:191], v[54:57]
	v_mfma_f32_16x16x32_bf16 v[50:53], v[180:183], v[188:191], v[50:53]
	ds_read_b128 v[188:191], v167 offset:0xc00
	s_waitcnt lgkmcnt(1)
	s_nop 0
	v_mfma_f32_16x16x32_bf16 v[46:49], v[168:171], v[184:187], v[46:49]
	v_mfma_f32_16x16x32_bf16 v[42:45], v[172:175], v[184:187], v[42:45]
	v_mfma_f32_16x16x32_bf16 v[38:41], v[176:179], v[184:187], v[38:41]
	v_mfma_f32_16x16x32_bf16 v[34:37], v[180:183], v[184:187], v[34:37]
	ds_read_b128 v[184:187], v167 offset:0x1000
	s_waitcnt lgkmcnt(1)
	s_nop 0
	v_mfma_f32_16x16x32_bf16 v[18:21], v[168:171], v[188:191], v[18:21]
	v_mfma_f32_16x16x32_bf16 v[22:25], v[172:175], v[188:191], v[22:25]
	v_mfma_f32_16x16x32_bf16 v[26:29], v[176:179], v[188:191], v[26:29]
	v_mfma_f32_16x16x32_bf16 v[30:33], v[180:183], v[188:191], v[30:33]
	ds_read_b128 v[188:191], v167 offset:0x1400
	s_waitcnt lgkmcnt(1)
	s_nop 0
	v_mfma_f32_16x16x32_bf16 v[88:91], v[168:171], v[184:187], v[88:91]
	v_mfma_f32_16x16x32_bf16 v[112:115], v[172:175], v[184:187], v[112:115]
	v_mfma_f32_16x16x32_bf16 v[108:111], v[176:179], v[184:187], v[108:111]
	v_mfma_f32_16x16x32_bf16 v[100:103], v[180:183], v[184:187], v[100:103]
	ds_read_b128 v[184:187], v167 offset:0x1800
	s_waitcnt lgkmcnt(1)
	s_nop 0
	v_mfma_f32_16x16x32_bf16 v[82:85], v[168:171], v[188:191], v[82:85]
	v_mfma_f32_16x16x32_bf16 v[92:95], v[172:175], v[188:191], v[92:95]
	v_mfma_f32_16x16x32_bf16 v[96:99], v[176:179], v[188:191], v[96:99]
	v_mfma_f32_16x16x32_bf16 v[104:107], v[180:183], v[188:191], v[104:107]
	ds_read_b128 v[188:191], v167 offset:0x1c00
	s_waitcnt lgkmcnt(1)
	s_nop 0
	v_mfma_f32_16x16x32_bf16 v[116:119], v[168:171], v[184:187], v[116:119]
	s_waitcnt lgkmcnt(0)
	v_mfma_f32_16x16x32_bf16 v[124:127], v[172:175], v[184:187], v[124:127]
	v_mfma_f32_16x16x32_bf16 v[132:135], v[176:179], v[184:187], v[132:135]
	v_mfma_f32_16x16x32_bf16 v[136:139], v[180:183], v[184:187], v[136:139]
	v_mfma_f32_16x16x32_bf16 v[120:123], v[168:171], v[188:191], v[120:123]
	v_mfma_f32_16x16x32_bf16 v[128:131], v[172:175], v[188:191], v[128:131]
	v_mfma_f32_16x16x32_bf16 v[140:143], v[176:179], v[188:191], v[140:143]
	v_mfma_f32_16x16x32_bf16 v[144:147], v[180:183], v[188:191], v[144:147]
	s_setprio 0
	s_waitcnt vmcnt(7)
	s_add_i32 s8, s6, 1
	s_cmp_lg_u32 s6, 2
	s_cselect_b32 s6, s8, 0
	s_cmp_gt_u32 s7, 13
	s_mov_b32 s8, s7
	s_waitcnt vmcnt(7)
	v_cvt_pk_bf16_f32 v156, v156, v160
	v_cvt_pk_bf16_f32 v157, v157, v161
	v_cvt_pk_bf16_f32 v158, v158, v162
	v_cvt_pk_bf16_f32 v159, v159, v163
	ds_write_b128 v166, v[156:159]
	s_cbranch_scc0 .LBB0_3448
	s_waitcnt vmcnt(0)
	s_mov_b64 s[6:7], 0
	s_branch .LBB0_3455

.LBB0_3453:
	s_add_i32 s9, s24, 2
	s_add_i32 s24, s24, 4
	s_min_u32 s24, s24, 15
	s_mul_i32 s25, s8, 0xa000
	s_lshl_b32 s64, s24, 6
	s_add_i32 s26, s25, 0xffff6000
	s_cmp_lg_u32 s8, 0
	s_cselect_b32 s26, s26, 0x14000
	s_add_i32 s26, s22, s26
	s_waitcnt lgkmcnt(0)
	s_barrier
	v_lshl_add_u64 v[124:125], v[200:201], 0, s[64:65]
	s_mov_b32 m0, s26
	s_nop 0
	global_load_lds_dwordx4 v[124:125], off
	v_lshl_add_u64 v[124:125], v[202:203], 0, s[64:65]
	s_add_i32 m0, s26, 0x400
	s_nop 0
	global_load_lds_dwordx4 v[124:125], off
	v_lshl_add_u64 v[124:125], v[204:205], 0, s[64:65]
	s_add_i32 m0, s26, 0x800
	s_nop 0
	global_load_lds_dwordx4 v[124:125], off
	v_lshl_add_u64 v[124:125], v[206:207], 0, s[64:65]
	s_add_i32 m0, s26, 0xc00
	s_nop 0
	global_load_lds_dwordx4 v[124:125], off
	v_lshl_add_u64 v[124:125], v[208:209], 0, s[64:65]
	s_add_i32 m0, s26, 0x1000
	s_lshl_b32 s64, s24, 18
	global_load_lds_dwordx4 v[124:125], off
	v_lshl_add_u64 v[124:125], v[210:211], 0, s[64:65]
	v_add_co_u32_e32 v128, vcc, s33, v124
	s_nop 1
	v_addc_co_u32_e32 v129, vcc, 0, v125, vcc
	global_load_dwordx4 v[124:127], v[124:125], off nt
	s_nop 0
	global_load_dwordx4 v[128:131], v[128:129], off nt
	v_add_u32_e32 v158, s25, v86
	ds_read2_b32 v[134:135], v232 offset0:0 offset1:0x84
	ds_read2_b32 v[136:137], v233 offset0:0 offset1:0x84
	ds_read2_b32 v[138:139], v232 offset0:16 offset1:0x94
	ds_read2_b32 v[140:141], v233 offset0:16 offset1:0x94
	ds_read2_b32 v[142:143], v232 offset0:32 offset1:0xa4
	ds_read2_b32 v[144:145], v233 offset0:32 offset1:0xa4
	ds_read2_b32 v[146:147], v232 offset0:48 offset1:0xb4
	ds_read2_b32 v[148:149], v233 offset0:48 offset1:0xb4
	ds_read_b128 v[150:153], v158 offset:0
	ds_read_b128 v[154:157], v158 offset:0x400
	s_nop 0
	s_waitcnt lgkmcnt(1)
	s_setprio 1
	v_mfma_f32_16x16x32_bf16 v[78:81], v[134:137], v[150:153], v[78:81]
	v_mfma_f32_16x16x32_bf16 v[74:77], v[138:141], v[150:153], v[74:77]
	v_mfma_f32_16x16x32_bf16 v[70:73], v[142:145], v[150:153], v[70:73]
	v_mfma_f32_16x16x32_bf16 v[66:69], v[146:149], v[150:153], v[66:69]
	ds_read_b128 v[150:153], v158 offset:0x800
	s_waitcnt lgkmcnt(1)
	s_nop 0
	v_mfma_f32_16x16x32_bf16 v[62:65], v[134:137], v[154:157], v[62:65]
	v_mfma_f32_16x16x32_bf16 v[58:61], v[138:141], v[154:157], v[58:61]
	v_mfma_f32_16x16x32_bf16 v[54:57], v[142:145], v[154:157], v[54:57]
	v_mfma_f32_16x16x32_bf16 v[50:53], v[146:149], v[154:157], v[50:53]
	ds_read_b128 v[154:157], v158 offset:0xc00
	s_waitcnt lgkmcnt(1)
	s_nop 0
	v_mfma_f32_16x16x32_bf16 v[46:49], v[134:137], v[150:153], v[46:49]
	v_mfma_f32_16x16x32_bf16 v[42:45], v[138:141], v[150:153], v[42:45]
	v_mfma_f32_16x16x32_bf16 v[38:41], v[142:145], v[150:153], v[38:41]
	v_mfma_f32_16x16x32_bf16 v[34:37], v[146:149], v[150:153], v[34:37]
	ds_read_b128 v[150:153], v158 offset:0x1000
	s_waitcnt lgkmcnt(1)
	s_nop 0
	v_mfma_f32_16x16x32_bf16 v[18:21], v[134:137], v[154:157], v[18:21]
	v_mfma_f32_16x16x32_bf16 v[22:25], v[138:141], v[154:157], v[22:25]
	v_mfma_f32_16x16x32_bf16 v[26:29], v[142:145], v[154:157], v[26:29]
	v_mfma_f32_16x16x32_bf16 v[30:33], v[146:149], v[154:157], v[30:33]
	ds_read_b128 v[154:157], v158 offset:0x1400
	s_waitcnt lgkmcnt(1)
	s_nop 0
	v_mfma_f32_16x16x32_bf16 v[88:91], v[134:137], v[150:153], v[88:91]
	s_waitcnt lgkmcnt(0)
	v_mfma_f32_16x16x32_bf16 v[112:115], v[138:141], v[150:153], v[112:115]
	v_mfma_f32_16x16x32_bf16 v[108:111], v[142:145], v[150:153], v[108:111]
	v_mfma_f32_16x16x32_bf16 v[100:103], v[146:149], v[150:153], v[100:103]
	v_mfma_f32_16x16x32_bf16 v[82:85], v[134:137], v[154:157], v[82:85]
	v_mfma_f32_16x16x32_bf16 v[92:95], v[138:141], v[154:157], v[92:95]
	v_mfma_f32_16x16x32_bf16 v[96:99], v[142:145], v[154:157], v[96:99]
	v_mfma_f32_16x16x32_bf16 v[104:107], v[146:149], v[154:157], v[104:107]
	s_setprio 0
	s_add_i32 s24, s8, 1
	s_cmp_lg_u32 s8, 2
	s_cselect_b32 s8, s24, 0
	s_min_u32 s24, s9, 12
	s_add_i32 s24, s24, 3
	s_mul_i32 s25, s8, 0xa000
	s_lshl_b32 s64, s24, 6
	s_add_i32 s26, s25, 0xffff6000
	s_cmp_lg_u32 s8, 0
	s_waitcnt vmcnt(7)
	v_cvt_pk_bf16_f32 v116, v116, v120
	v_add_u32_e32 v120, 0x20100, v132
	s_cselect_b32 s26, s26, 0x14000
	v_cvt_pk_bf16_f32 v117, v117, v121
	v_cvt_pk_bf16_f32 v118, v118, v122
	v_cvt_pk_bf16_f32 v119, v119, v123
	ds_write_b128 v120, v[116:119]
	s_add_i32 s26, s22, s26
	s_waitcnt lgkmcnt(0)
	s_barrier
	v_lshl_add_u64 v[116:117], v[200:201], 0, s[64:65]
	s_mov_b32 m0, s26
	s_nop 0
	global_load_lds_dwordx4 v[116:117], off
	v_lshl_add_u64 v[116:117], v[202:203], 0, s[64:65]
	s_add_i32 m0, s26, 0x400
	s_nop 0
	global_load_lds_dwordx4 v[116:117], off
	v_lshl_add_u64 v[116:117], v[204:205], 0, s[64:65]
	s_add_i32 m0, s26, 0x800
	s_nop 0
	global_load_lds_dwordx4 v[116:117], off
	v_lshl_add_u64 v[116:117], v[206:207], 0, s[64:65]
	s_add_i32 m0, s26, 0xc00
	s_nop 0
	global_load_lds_dwordx4 v[116:117], off
	v_lshl_add_u64 v[116:117], v[208:209], 0, s[64:65]
	s_lshl_b32 s64, s24, 18
	s_add_i32 m0, s26, 0x1000
	v_lshl_add_u64 v[120:121], v[210:211], 0, s[64:65]
	global_load_lds_dwordx4 v[116:117], off
	global_load_dwordx4 v[116:119], v[120:121], off nt
	v_add_co_u32_e32 v120, vcc, s33, v120
	s_nop 1
	v_addc_co_u32_e32 v121, vcc, 0, v121, vcc
	global_load_dwordx4 v[120:123], v[120:121], off nt
	v_add_u32_e32 v158, s25, v86
	ds_read2_b32 v[134:135], v234 offset0:0 offset1:0x84
	ds_read2_b32 v[136:137], v235 offset0:0 offset1:0x84
	ds_read2_b32 v[138:139], v234 offset0:16 offset1:0x94
	ds_read2_b32 v[140:141], v235 offset0:16 offset1:0x94
	ds_read2_b32 v[142:143], v234 offset0:32 offset1:0xa4
	ds_read2_b32 v[144:145], v235 offset0:32 offset1:0xa4
	ds_read2_b32 v[146:147], v234 offset0:48 offset1:0xb4
	ds_read2_b32 v[148:149], v235 offset0:48 offset1:0xb4
	ds_read_b128 v[150:153], v158 offset:0
	ds_read_b128 v[154:157], v158 offset:0x400
	s_nop 0
	s_waitcnt lgkmcnt(1)
	s_setprio 1
	v_mfma_f32_16x16x32_bf16 v[78:81], v[134:137], v[150:153], v[78:81]
	v_mfma_f32_16x16x32_bf16 v[74:77], v[138:141], v[150:153], v[74:77]
	v_mfma_f32_16x16x32_bf16 v[70:73], v[142:145], v[150:153], v[70:73]
	v_mfma_f32_16x16x32_bf16 v[66:69], v[146:149], v[150:153], v[66:69]
	ds_read_b128 v[150:153], v158 offset:0x800
	s_waitcnt lgkmcnt(1)
	s_nop 0
	v_mfma_f32_16x16x32_bf16 v[62:65], v[134:137], v[154:157], v[62:65]
	v_mfma_f32_16x16x32_bf16 v[58:61], v[138:141], v[154:157], v[58:61]
	v_mfma_f32_16x16x32_bf16 v[54:57], v[142:145], v[154:157], v[54:57]
	v_mfma_f32_16x16x32_bf16 v[50:53], v[146:149], v[154:157], v[50:53]
	ds_read_b128 v[154:157], v158 offset:0xc00
	s_waitcnt lgkmcnt(1)
	s_nop 0
	v_mfma_f32_16x16x32_bf16 v[46:49], v[134:137], v[150:153], v[46:49]
	v_mfma_f32_16x16x32_bf16 v[42:45], v[138:141], v[150:153], v[42:45]
	v_mfma_f32_16x16x32_bf16 v[38:41], v[142:145], v[150:153], v[38:41]
	v_mfma_f32_16x16x32_bf16 v[34:37], v[146:149], v[150:153], v[34:37]
	ds_read_b128 v[150:153], v158 offset:0x1000
	s_waitcnt lgkmcnt(1)
	s_nop 0
	v_mfma_f32_16x16x32_bf16 v[18:21], v[134:137], v[154:157], v[18:21]
	v_mfma_f32_16x16x32_bf16 v[22:25], v[138:141], v[154:157], v[22:25]
	v_mfma_f32_16x16x32_bf16 v[26:29], v[142:145], v[154:157], v[26:29]
	v_mfma_f32_16x16x32_bf16 v[30:33], v[146:149], v[154:157], v[30:33]
	ds_read_b128 v[154:157], v158 offset:0x1400
	s_waitcnt lgkmcnt(1)
	s_nop 0
	v_mfma_f32_16x16x32_bf16 v[88:91], v[134:137], v[150:153], v[88:91]
	s_waitcnt lgkmcnt(0)
	v_mfma_f32_16x16x32_bf16 v[112:115], v[138:141], v[150:153], v[112:115]
	v_mfma_f32_16x16x32_bf16 v[108:111], v[142:145], v[150:153], v[108:111]
	v_mfma_f32_16x16x32_bf16 v[100:103], v[146:149], v[150:153], v[100:103]
	v_mfma_f32_16x16x32_bf16 v[82:85], v[134:137], v[154:157], v[82:85]
	v_mfma_f32_16x16x32_bf16 v[92:95], v[138:141], v[154:157], v[92:95]
	v_mfma_f32_16x16x32_bf16 v[96:99], v[142:145], v[154:157], v[96:99]
	v_mfma_f32_16x16x32_bf16 v[104:107], v[146:149], v[154:157], v[104:107]
	s_setprio 0
	s_waitcnt vmcnt(7)
	s_add_i32 s24, s8, 1
	s_cmp_lg_u32 s8, 2
	s_cselect_b32 s8, s24, 0
	s_cmp_gt_u32 s9, 13
	s_mov_b32 s24, s9
	s_waitcnt vmcnt(7)
	v_cvt_pk_bf16_f32 v124, v124, v128
	v_cvt_pk_bf16_f32 v125, v125, v129
	v_cvt_pk_bf16_f32 v126, v126, v130
	v_cvt_pk_bf16_f32 v127, v127, v131
	ds_write_b128 v133, v[124:127]
	s_cbranch_scc0 .LBB0_3453
	s_waitcnt vmcnt(0)
	v_mov_b32_e32 v119, 0
	v_mov_b32_e32 v118, v119
	v_mov_b32_e32 v117, v119
	v_mov_b32_e32 v116, v119
	v_mov_b32_e32 v127, v119
	v_mov_b32_e32 v126, v119
	v_mov_b32_e32 v125, v119
	v_mov_b32_e32 v124, v119
	v_mov_b32_e32 v135, v119
	v_mov_b32_e32 v134, v119
	v_mov_b32_e32 v133, v119
	v_mov_b32_e32 v132, v119
	v_mov_b32_e32 v139, v119
	v_mov_b32_e32 v138, v119
	v_mov_b32_e32 v137, v119
	v_mov_b32_e32 v136, v119
	v_mov_b32_e32 v123, v119
	v_mov_b32_e32 v122, v119
	v_mov_b32_e32 v121, v119
	v_mov_b32_e32 v120, v119
	v_mov_b32_e32 v131, v119
	v_mov_b32_e32 v130, v119
	v_mov_b32_e32 v129, v119
	v_mov_b32_e32 v128, v119
	v_mov_b32_e32 v143, v119
	v_mov_b32_e32 v142, v119
	v_mov_b32_e32 v141, v119
	v_mov_b32_e32 v140, v119
	v_mov_b32_e32 v147, v119
	v_mov_b32_e32 v146, v119
	v_mov_b32_e32 v145, v119
	v_mov_b32_e32 v144, v119

.LBB0_3459:
	s_add_i32 s4, s8, 2
	s_add_i32 s8, s8, 4
	s_min_u32 s8, s8, 15
	s_mul_i32 s9, s5, 0xa000
	s_lshl_b32 s64, s8, 6
	s_add_i32 s24, s9, 0xffff6000
	s_cmp_lg_u32 s5, 0
	s_cselect_b32 s24, s24, 0x14000
	s_add_i32 s24, s22, s24
	s_waitcnt lgkmcnt(0)
	s_barrier
	v_lshl_add_u64 v[92:93], v[200:201], 0, s[64:65]
	s_mov_b32 m0, s24
	s_nop 0
	global_load_lds_dwordx4 v[92:93], off
	v_lshl_add_u64 v[92:93], v[202:203], 0, s[64:65]
	s_add_i32 m0, s24, 0x400
	s_nop 0
	global_load_lds_dwordx4 v[92:93], off
	v_lshl_add_u64 v[92:93], v[204:205], 0, s[64:65]
	s_add_i32 m0, s24, 0x800
	s_nop 0
	global_load_lds_dwordx4 v[92:93], off
	v_lshl_add_u64 v[92:93], v[206:207], 0, s[64:65]
	s_add_i32 m0, s24, 0xc00
	s_nop 0
	global_load_lds_dwordx4 v[92:93], off
	v_lshl_add_u64 v[92:93], v[208:209], 0, s[64:65]
	s_add_i32 m0, s24, 0x1000
	s_lshl_b32 s64, s8, 18
	global_load_lds_dwordx4 v[92:93], off
	v_lshl_add_u64 v[92:93], v[210:211], 0, s[64:65]
	v_add_co_u32_e32 v96, vcc, s33, v92
	s_nop 1
	v_addc_co_u32_e32 v97, vcc, 0, v93, vcc
	global_load_dwordx4 v[92:95], v[92:93], off nt
	s_nop 0
	global_load_dwordx4 v[96:99], v[96:97], off nt
	v_add_u32_e32 v126, s9, v86
	ds_read2_b32 v[102:103], v232 offset0:0 offset1:0x84
	ds_read2_b32 v[104:105], v233 offset0:0 offset1:0x84
	ds_read2_b32 v[106:107], v232 offset0:16 offset1:0x94
	ds_read2_b32 v[108:109], v233 offset0:16 offset1:0x94
	ds_read2_b32 v[110:111], v232 offset0:32 offset1:0xa4
	ds_read2_b32 v[112:113], v233 offset0:32 offset1:0xa4
	ds_read2_b32 v[114:115], v232 offset0:48 offset1:0xb4
	ds_read2_b32 v[116:117], v233 offset0:48 offset1:0xb4
	ds_read_b128 v[118:121], v126 offset:0
	ds_read_b128 v[122:125], v126 offset:0x400
	s_nop 0
	s_waitcnt lgkmcnt(1)
	s_setprio 1
	v_mfma_f32_16x16x32_bf16 v[78:81], v[102:105], v[118:121], v[78:81]
	v_mfma_f32_16x16x32_bf16 v[74:77], v[106:109], v[118:121], v[74:77]
	v_mfma_f32_16x16x32_bf16 v[70:73], v[110:113], v[118:121], v[70:73]
	v_mfma_f32_16x16x32_bf16 v[66:69], v[114:117], v[118:121], v[66:69]
	ds_read_b128 v[118:121], v126 offset:0x800
	s_waitcnt lgkmcnt(1)
	s_nop 0
	v_mfma_f32_16x16x32_bf16 v[62:65], v[102:105], v[122:125], v[62:65]
	v_mfma_f32_16x16x32_bf16 v[58:61], v[106:109], v[122:125], v[58:61]
	v_mfma_f32_16x16x32_bf16 v[54:57], v[110:113], v[122:125], v[54:57]
	v_mfma_f32_16x16x32_bf16 v[50:53], v[114:117], v[122:125], v[50:53]
	ds_read_b128 v[122:125], v126 offset:0xc00
	s_waitcnt lgkmcnt(1)
	s_nop 0
	v_mfma_f32_16x16x32_bf16 v[46:49], v[102:105], v[118:121], v[46:49]
	s_waitcnt lgkmcnt(0)
	v_mfma_f32_16x16x32_bf16 v[42:45], v[106:109], v[118:121], v[42:45]
	v_mfma_f32_16x16x32_bf16 v[38:41], v[110:113], v[118:121], v[38:41]
	v_mfma_f32_16x16x32_bf16 v[34:37], v[114:117], v[118:121], v[34:37]
	v_mfma_f32_16x16x32_bf16 v[18:21], v[102:105], v[122:125], v[18:21]
	v_mfma_f32_16x16x32_bf16 v[22:25], v[106:109], v[122:125], v[22:25]
	v_mfma_f32_16x16x32_bf16 v[26:29], v[110:113], v[122:125], v[26:29]
	v_mfma_f32_16x16x32_bf16 v[30:33], v[114:117], v[122:125], v[30:33]
	s_setprio 0
	s_add_i32 s8, s5, 1
	s_cmp_lg_u32 s5, 2
	s_cselect_b32 s5, s8, 0
	s_min_u32 s8, s4, 12
	s_add_i32 s8, s8, 3
	s_mul_i32 s9, s5, 0xa000
	s_lshl_b32 s64, s8, 6
	s_add_i32 s24, s9, 0xffff6000
	s_cmp_lg_u32 s5, 0
	s_waitcnt vmcnt(7)
	v_cvt_pk_bf16_f32 v82, v82, v88
	v_add_u32_e32 v88, 0x20100, v100
	s_cselect_b32 s24, s24, 0x14000
	v_cvt_pk_bf16_f32 v83, v83, v89
	v_cvt_pk_bf16_f32 v84, v84, v90
	v_cvt_pk_bf16_f32 v85, v85, v91
	ds_write_b128 v88, v[82:85]
	s_add_i32 s24, s22, s24
	s_waitcnt lgkmcnt(0)
	s_barrier
	v_lshl_add_u64 v[82:83], v[200:201], 0, s[64:65]
	s_mov_b32 m0, s24
	s_nop 0
	global_load_lds_dwordx4 v[82:83], off
	v_lshl_add_u64 v[82:83], v[202:203], 0, s[64:65]
	s_add_i32 m0, s24, 0x400
	s_nop 0
	global_load_lds_dwordx4 v[82:83], off
	v_lshl_add_u64 v[82:83], v[204:205], 0, s[64:65]
	s_add_i32 m0, s24, 0x800
	s_nop 0
	global_load_lds_dwordx4 v[82:83], off
	v_lshl_add_u64 v[82:83], v[206:207], 0, s[64:65]
	s_add_i32 m0, s24, 0xc00
	s_nop 0
	global_load_lds_dwordx4 v[82:83], off
	v_lshl_add_u64 v[82:83], v[208:209], 0, s[64:65]
	s_lshl_b32 s64, s8, 18
	s_add_i32 m0, s24, 0x1000
	v_lshl_add_u64 v[88:89], v[210:211], 0, s[64:65]
	global_load_lds_dwordx4 v[82:83], off
	global_load_dwordx4 v[82:85], v[88:89], off nt
	v_add_co_u32_e32 v88, vcc, s33, v88
	s_nop 1
	v_addc_co_u32_e32 v89, vcc, 0, v89, vcc
	global_load_dwordx4 v[88:91], v[88:89], off nt
	v_add_u32_e32 v126, s9, v86
	ds_read2_b32 v[102:103], v234 offset0:0 offset1:0x84
	ds_read2_b32 v[104:105], v235 offset0:0 offset1:0x84
	ds_read2_b32 v[106:107], v234 offset0:16 offset1:0x94
	ds_read2_b32 v[108:109], v235 offset0:16 offset1:0x94
	ds_read2_b32 v[110:111], v234 offset0:32 offset1:0xa4
	ds_read2_b32 v[112:113], v235 offset0:32 offset1:0xa4
	ds_read2_b32 v[114:115], v234 offset0:48 offset1:0xb4
	ds_read2_b32 v[116:117], v235 offset0:48 offset1:0xb4
	ds_read_b128 v[118:121], v126 offset:0
	ds_read_b128 v[122:125], v126 offset:0x400
	s_nop 0
	s_waitcnt lgkmcnt(1)
	s_setprio 1
	v_mfma_f32_16x16x32_bf16 v[78:81], v[102:105], v[118:121], v[78:81]
	v_mfma_f32_16x16x32_bf16 v[74:77], v[106:109], v[118:121], v[74:77]
	v_mfma_f32_16x16x32_bf16 v[70:73], v[110:113], v[118:121], v[70:73]
	v_mfma_f32_16x16x32_bf16 v[66:69], v[114:117], v[118:121], v[66:69]
	ds_read_b128 v[118:121], v126 offset:0x800
	s_waitcnt lgkmcnt(1)
	s_nop 0
	v_mfma_f32_16x16x32_bf16 v[62:65], v[102:105], v[122:125], v[62:65]
	v_mfma_f32_16x16x32_bf16 v[58:61], v[106:109], v[122:125], v[58:61]
	v_mfma_f32_16x16x32_bf16 v[54:57], v[110:113], v[122:125], v[54:57]
	v_mfma_f32_16x16x32_bf16 v[50:53], v[114:117], v[122:125], v[50:53]
	ds_read_b128 v[122:125], v126 offset:0xc00
	s_waitcnt lgkmcnt(1)
	s_nop 0
	v_mfma_f32_16x16x32_bf16 v[46:49], v[102:105], v[118:121], v[46:49]
	s_waitcnt lgkmcnt(0)
	v_mfma_f32_16x16x32_bf16 v[42:45], v[106:109], v[118:121], v[42:45]
	v_mfma_f32_16x16x32_bf16 v[38:41], v[110:113], v[118:121], v[38:41]
	v_mfma_f32_16x16x32_bf16 v[34:37], v[114:117], v[118:121], v[34:37]
	v_mfma_f32_16x16x32_bf16 v[18:21], v[102:105], v[122:125], v[18:21]
	v_mfma_f32_16x16x32_bf16 v[22:25], v[106:109], v[122:125], v[22:25]
	v_mfma_f32_16x16x32_bf16 v[26:29], v[110:113], v[122:125], v[26:29]
	v_mfma_f32_16x16x32_bf16 v[30:33], v[114:117], v[122:125], v[30:33]
	s_setprio 0
	s_waitcnt vmcnt(7)
	s_add_i32 s8, s5, 1
	s_cmp_lg_u32 s5, 2
	s_cselect_b32 s5, s8, 0
	s_cmp_gt_u32 s4, 13
	s_mov_b32 s8, s4
	s_waitcnt vmcnt(7)
	v_cvt_pk_bf16_f32 v92, v92, v96
	v_cvt_pk_bf16_f32 v93, v93, v97
	v_cvt_pk_bf16_f32 v94, v94, v98
	v_cvt_pk_bf16_f32 v95, v95, v99
	ds_write_b128 v101, v[92:95]
	s_cbranch_scc0 .LBB0_3459
	s_waitcnt vmcnt(0)
	s_mov_b64 s[8:9], 0

.LBB0_3466:
	s_add_i32 s5, s6, 2
	s_add_i32 s6, s6, 4
	s_min_u32 s6, s6, 15
	s_mul_i32 s7, s4, 0xa000
	s_lshl_b32 s64, s6, 6
	s_add_i32 s8, s7, 0xffff6000
	s_cmp_lg_u32 s4, 0
	s_cselect_b32 s8, s8, 0x14000
	s_add_i32 s8, s22, s8
	s_waitcnt lgkmcnt(0)
	s_barrier
	v_lshl_add_u64 v[188:189], v[200:201], 0, s[64:65]
	s_mov_b32 m0, s8
	s_nop 0
	global_load_lds_dwordx4 v[188:189], off
	v_lshl_add_u64 v[188:189], v[202:203], 0, s[64:65]
	s_add_i32 m0, s8, 0x400
	s_nop 0
	global_load_lds_dwordx4 v[188:189], off
	v_lshl_add_u64 v[188:189], v[204:205], 0, s[64:65]
	s_add_i32 m0, s8, 0x800
	s_nop 0
	global_load_lds_dwordx4 v[188:189], off
	v_lshl_add_u64 v[188:189], v[206:207], 0, s[64:65]
	s_add_i32 m0, s8, 0xc00
	s_nop 0
	global_load_lds_dwordx4 v[188:189], off
	v_lshl_add_u64 v[188:189], v[208:209], 0, s[64:65]
	s_add_i32 m0, s8, 0x1000
	s_lshl_b32 s64, s6, 18
	global_load_lds_dwordx4 v[188:189], off
	v_lshl_add_u64 v[188:189], v[210:211], 0, s[64:65]
	v_add_co_u32_e32 v192, vcc, s33, v188
	s_nop 1
	v_addc_co_u32_e32 v193, vcc, 0, v189, vcc
	global_load_dwordx4 v[188:191], v[188:189], off nt
	s_nop 0
	global_load_dwordx4 v[192:195], v[192:193], off nt
	v_add_u32_e32 v216, s7, v86
	ds_read2_b32 v[196:197], v232 offset0:0 offset1:0x84
	ds_read2_b32 v[198:199], v233 offset0:0 offset1:0x84
	ds_read2_b32 v[222:223], v232 offset0:16 offset1:0x94
	ds_read2_b32 v[224:225], v233 offset0:16 offset1:0x94
	ds_read2_b32 v[226:227], v232 offset0:32 offset1:0xa4
	ds_read2_b32 v[228:229], v233 offset0:32 offset1:0xa4
	ds_read2_b32 v[238:239], v232 offset0:48 offset1:0xb4
	ds_read2_b32 v[240:241], v233 offset0:48 offset1:0xb4
	ds_read_b128 v[242:245], v216 offset:0
	ds_read_b128 v[246:249], v216 offset:0x400
	s_nop 0
	s_waitcnt lgkmcnt(1)
	s_setprio 1
	v_mfma_f32_16x16x32_bf16 v[78:81], v[196:199], v[242:245], v[78:81]
	v_mfma_f32_16x16x32_bf16 v[74:77], v[222:225], v[242:245], v[74:77]
	v_mfma_f32_16x16x32_bf16 v[70:73], v[226:229], v[242:245], v[70:73]
	v_mfma_f32_16x16x32_bf16 v[66:69], v[238:241], v[242:245], v[66:69]
	ds_read_b128 v[242:245], v216 offset:0x800
	s_waitcnt lgkmcnt(1)
	s_nop 0
	v_mfma_f32_16x16x32_bf16 v[62:65], v[196:199], v[246:249], v[62:65]
	v_mfma_f32_16x16x32_bf16 v[58:61], v[222:225], v[246:249], v[58:61]
	v_mfma_f32_16x16x32_bf16 v[54:57], v[226:229], v[246:249], v[54:57]
	v_mfma_f32_16x16x32_bf16 v[50:53], v[238:241], v[246:249], v[50:53]
	ds_read_b128 v[246:249], v216 offset:0xc00
	s_waitcnt lgkmcnt(1)
	s_nop 0
	v_mfma_f32_16x16x32_bf16 v[46:49], v[196:199], v[242:245], v[46:49]
	v_mfma_f32_16x16x32_bf16 v[42:45], v[222:225], v[242:245], v[42:45]
	v_mfma_f32_16x16x32_bf16 v[38:41], v[226:229], v[242:245], v[38:41]
	v_mfma_f32_16x16x32_bf16 v[34:37], v[238:241], v[242:245], v[34:37]
	ds_read_b128 v[242:245], v216 offset:0x1000
	s_waitcnt lgkmcnt(1)
	s_nop 0
	v_mfma_f32_16x16x32_bf16 v[18:21], v[196:199], v[246:249], v[18:21]
	v_mfma_f32_16x16x32_bf16 v[22:25], v[222:225], v[246:249], v[22:25]
	v_mfma_f32_16x16x32_bf16 v[26:29], v[226:229], v[246:249], v[26:29]
	v_mfma_f32_16x16x32_bf16 v[30:33], v[238:241], v[246:249], v[30:33]
	ds_read_b128 v[246:249], v216 offset:0x1400
	s_waitcnt lgkmcnt(1)
	s_nop 0
	v_mfma_f32_16x16x32_bf16 v[88:91], v[196:199], v[242:245], v[88:91]
	v_mfma_f32_16x16x32_bf16 v[112:115], v[222:225], v[242:245], v[112:115]
	v_mfma_f32_16x16x32_bf16 v[108:111], v[226:229], v[242:245], v[108:111]
	v_mfma_f32_16x16x32_bf16 v[100:103], v[238:241], v[242:245], v[100:103]
	ds_read_b128 v[242:245], v216 offset:0x1800
	s_waitcnt lgkmcnt(1)
	s_nop 0
	v_mfma_f32_16x16x32_bf16 v[82:85], v[196:199], v[246:249], v[82:85]
	v_mfma_f32_16x16x32_bf16 v[92:95], v[222:225], v[246:249], v[92:95]
	v_mfma_f32_16x16x32_bf16 v[96:99], v[226:229], v[246:249], v[96:99]
	v_mfma_f32_16x16x32_bf16 v[104:107], v[238:241], v[246:249], v[104:107]
	ds_read_b128 v[246:249], v216 offset:0x1c00
	s_waitcnt lgkmcnt(1)
	s_nop 0
	v_mfma_f32_16x16x32_bf16 v[116:119], v[196:199], v[242:245], v[116:119]
	v_mfma_f32_16x16x32_bf16 v[124:127], v[222:225], v[242:245], v[124:127]
	v_mfma_f32_16x16x32_bf16 v[132:135], v[226:229], v[242:245], v[132:135]
	v_mfma_f32_16x16x32_bf16 v[136:139], v[238:241], v[242:245], v[136:139]
	ds_read_b128 v[242:245], v216 offset:0x2000
	s_waitcnt lgkmcnt(1)
	s_nop 0
	v_mfma_f32_16x16x32_bf16 v[120:123], v[196:199], v[246:249], v[120:123]
	v_mfma_f32_16x16x32_bf16 v[128:131], v[222:225], v[246:249], v[128:131]
	v_mfma_f32_16x16x32_bf16 v[140:143], v[226:229], v[246:249], v[140:143]
	v_mfma_f32_16x16x32_bf16 v[144:147], v[238:241], v[246:249], v[144:147]
	ds_read_b128 v[246:249], v216 offset:0x2400
	s_waitcnt lgkmcnt(1)
	s_nop 0
	v_mfma_f32_16x16x32_bf16 v[148:151], v[196:199], v[242:245], v[148:151]
	s_waitcnt lgkmcnt(0)
	v_mfma_f32_16x16x32_bf16 v[176:179], v[222:225], v[242:245], v[176:179]
	v_mfma_f32_16x16x32_bf16 v[172:175], v[226:229], v[242:245], v[172:175]
	v_mfma_f32_16x16x32_bf16 v[168:171], v[238:241], v[242:245], v[168:171]
	v_mfma_f32_16x16x32_bf16 v[164:167], v[196:199], v[246:249], v[164:167]
	v_mfma_f32_16x16x32_bf16 v[160:163], v[222:225], v[246:249], v[160:163]
	v_mfma_f32_16x16x32_bf16 v[156:159], v[226:229], v[246:249], v[156:159]
	v_mfma_f32_16x16x32_bf16 v[152:155], v[238:241], v[246:249], v[152:155]
	s_setprio 0
	s_add_i32 s6, s4, 1
	s_cmp_lg_u32 s4, 2
	s_cselect_b32 s4, s6, 0
	s_min_u32 s6, s5, 12
	s_add_i32 s6, s6, 3
	s_mul_i32 s7, s4, 0xa000
	s_lshl_b32 s64, s6, 6
	s_add_i32 s8, s7, 0xffff6000
	s_cmp_lg_u32 s4, 0
	s_waitcnt vmcnt(7)
	v_cvt_pk_bf16_f32 v180, v180, v184
	v_add_u32_e32 v184, 0x20100, v236
	s_cselect_b32 s8, s8, 0x14000
	v_cvt_pk_bf16_f32 v181, v181, v185
	v_cvt_pk_bf16_f32 v182, v182, v186
	v_cvt_pk_bf16_f32 v183, v183, v187
	ds_write_b128 v184, v[180:183]
	s_add_i32 s8, s22, s8
	s_waitcnt lgkmcnt(0)
	s_barrier
	v_lshl_add_u64 v[180:181], v[200:201], 0, s[64:65]
	s_mov_b32 m0, s8
	s_nop 0
	global_load_lds_dwordx4 v[180:181], off
	v_lshl_add_u64 v[180:181], v[202:203], 0, s[64:65]
	s_add_i32 m0, s8, 0x400
	s_nop 0
	global_load_lds_dwordx4 v[180:181], off
	v_lshl_add_u64 v[180:181], v[204:205], 0, s[64:65]
	s_add_i32 m0, s8, 0x800
	s_nop 0
	global_load_lds_dwordx4 v[180:181], off
	v_lshl_add_u64 v[180:181], v[206:207], 0, s[64:65]
	s_add_i32 m0, s8, 0xc00
	s_nop 0
	global_load_lds_dwordx4 v[180:181], off
	v_lshl_add_u64 v[180:181], v[208:209], 0, s[64:65]
	s_lshl_b32 s64, s6, 18
	s_add_i32 m0, s8, 0x1000
	v_lshl_add_u64 v[184:185], v[210:211], 0, s[64:65]
	global_load_lds_dwordx4 v[180:181], off
	global_load_dwordx4 v[180:183], v[184:185], off nt
	v_add_co_u32_e32 v184, vcc, s33, v184
	s_nop 1
	v_addc_co_u32_e32 v185, vcc, 0, v185, vcc
	global_load_dwordx4 v[184:187], v[184:185], off nt
	v_add_u32_e32 v216, s7, v86
	ds_read2_b32 v[196:197], v234 offset0:0 offset1:0x84
	ds_read2_b32 v[198:199], v235 offset0:0 offset1:0x84
	ds_read2_b32 v[222:223], v234 offset0:16 offset1:0x94
	ds_read2_b32 v[224:225], v235 offset0:16 offset1:0x94
	ds_read2_b32 v[226:227], v234 offset0:32 offset1:0xa4
	ds_read2_b32 v[228:229], v235 offset0:32 offset1:0xa4
	ds_read2_b32 v[238:239], v234 offset0:48 offset1:0xb4
	ds_read2_b32 v[240:241], v235 offset0:48 offset1:0xb4
	ds_read_b128 v[242:245], v216 offset:0
	ds_read_b128 v[246:249], v216 offset:0x400
	s_nop 0
	s_waitcnt lgkmcnt(1)
	s_setprio 1
	v_mfma_f32_16x16x32_bf16 v[78:81], v[196:199], v[242:245], v[78:81]
	v_mfma_f32_16x16x32_bf16 v[74:77], v[222:225], v[242:245], v[74:77]
	v_mfma_f32_16x16x32_bf16 v[70:73], v[226:229], v[242:245], v[70:73]
	v_mfma_f32_16x16x32_bf16 v[66:69], v[238:241], v[242:245], v[66:69]
	ds_read_b128 v[242:245], v216 offset:0x800
	s_waitcnt lgkmcnt(1)
	s_nop 0
	v_mfma_f32_16x16x32_bf16 v[62:65], v[196:199], v[246:249], v[62:65]
	v_mfma_f32_16x16x32_bf16 v[58:61], v[222:225], v[246:249], v[58:61]
	v_mfma_f32_16x16x32_bf16 v[54:57], v[226:229], v[246:249], v[54:57]
	v_mfma_f32_16x16x32_bf16 v[50:53], v[238:241], v[246:249], v[50:53]
	ds_read_b128 v[246:249], v216 offset:0xc00
	s_waitcnt lgkmcnt(1)
	s_nop 0
	v_mfma_f32_16x16x32_bf16 v[46:49], v[196:199], v[242:245], v[46:49]
	v_mfma_f32_16x16x32_bf16 v[42:45], v[222:225], v[242:245], v[42:45]
	v_mfma_f32_16x16x32_bf16 v[38:41], v[226:229], v[242:245], v[38:41]
	v_mfma_f32_16x16x32_bf16 v[34:37], v[238:241], v[242:245], v[34:37]
	ds_read_b128 v[242:245], v216 offset:0x1000
	s_waitcnt lgkmcnt(1)
	s_nop 0
	v_mfma_f32_16x16x32_bf16 v[18:21], v[196:199], v[246:249], v[18:21]
	v_mfma_f32_16x16x32_bf16 v[22:25], v[222:225], v[246:249], v[22:25]
	v_mfma_f32_16x16x32_bf16 v[26:29], v[226:229], v[246:249], v[26:29]
	v_mfma_f32_16x16x32_bf16 v[30:33], v[238:241], v[246:249], v[30:33]
	ds_read_b128 v[246:249], v216 offset:0x1400
	s_waitcnt lgkmcnt(1)
	s_nop 0
	v_mfma_f32_16x16x32_bf16 v[88:91], v[196:199], v[242:245], v[88:91]
	v_mfma_f32_16x16x32_bf16 v[112:115], v[222:225], v[242:245], v[112:115]
	v_mfma_f32_16x16x32_bf16 v[108:111], v[226:229], v[242:245], v[108:111]
	v_mfma_f32_16x16x32_bf16 v[100:103], v[238:241], v[242:245], v[100:103]
	ds_read_b128 v[242:245], v216 offset:0x1800
	s_waitcnt lgkmcnt(1)
	s_nop 0
	v_mfma_f32_16x16x32_bf16 v[82:85], v[196:199], v[246:249], v[82:85]
	v_mfma_f32_16x16x32_bf16 v[92:95], v[222:225], v[246:249], v[92:95]
	v_mfma_f32_16x16x32_bf16 v[96:99], v[226:229], v[246:249], v[96:99]
	v_mfma_f32_16x16x32_bf16 v[104:107], v[238:241], v[246:249], v[104:107]
	ds_read_b128 v[246:249], v216 offset:0x1c00
	s_waitcnt lgkmcnt(1)
	s_nop 0
	v_mfma_f32_16x16x32_bf16 v[116:119], v[196:199], v[242:245], v[116:119]
	v_mfma_f32_16x16x32_bf16 v[124:127], v[222:225], v[242:245], v[124:127]
	v_mfma_f32_16x16x32_bf16 v[132:135], v[226:229], v[242:245], v[132:135]
	v_mfma_f32_16x16x32_bf16 v[136:139], v[238:241], v[242:245], v[136:139]
	ds_read_b128 v[242:245], v216 offset:0x2000
	s_waitcnt lgkmcnt(1)
	s_nop 0
	v_mfma_f32_16x16x32_bf16 v[120:123], v[196:199], v[246:249], v[120:123]
	v_mfma_f32_16x16x32_bf16 v[128:131], v[222:225], v[246:249], v[128:131]
	v_mfma_f32_16x16x32_bf16 v[140:143], v[226:229], v[246:249], v[140:143]
	v_mfma_f32_16x16x32_bf16 v[144:147], v[238:241], v[246:249], v[144:147]
	ds_read_b128 v[246:249], v216 offset:0x2400
	s_waitcnt lgkmcnt(1)
	s_nop 0
	v_mfma_f32_16x16x32_bf16 v[148:151], v[196:199], v[242:245], v[148:151]
	s_waitcnt lgkmcnt(0)
	v_mfma_f32_16x16x32_bf16 v[176:179], v[222:225], v[242:245], v[176:179]
	v_mfma_f32_16x16x32_bf16 v[172:175], v[226:229], v[242:245], v[172:175]
	v_mfma_f32_16x16x32_bf16 v[168:171], v[238:241], v[242:245], v[168:171]
	v_mfma_f32_16x16x32_bf16 v[164:167], v[196:199], v[246:249], v[164:167]
	v_mfma_f32_16x16x32_bf16 v[160:163], v[222:225], v[246:249], v[160:163]
	v_mfma_f32_16x16x32_bf16 v[156:159], v[226:229], v[246:249], v[156:159]
	v_mfma_f32_16x16x32_bf16 v[152:155], v[238:241], v[246:249], v[152:155]
	s_setprio 0
	s_waitcnt vmcnt(7)
	s_add_i32 s6, s4, 1
	s_cmp_lg_u32 s4, 2
	s_cselect_b32 s4, s6, 0
	s_cmp_gt_u32 s5, 13
	s_mov_b32 s6, s5
	s_waitcnt vmcnt(7)
	v_cvt_pk_bf16_f32 v188, v188, v192
	v_cvt_pk_bf16_f32 v189, v189, v193
	v_cvt_pk_bf16_f32 v190, v190, v194
	v_cvt_pk_bf16_f32 v191, v191, v195
	ds_write_b128 v237, v[188:191]
	s_cbranch_scc0 .LBB0_3466
	s_waitcnt vmcnt(0)
	s_mov_b64 s[4:5], 0

.LBB0_3470:
	s_add_i32 s4, s6, 2
	s_add_i32 s6, s6, 4
	s_min_u32 s6, s6, 15
	s_mul_i32 s7, s5, 0xa000
	s_lshl_b32 s64, s6, 6
	s_add_i32 s8, s7, 0xffff6000
	s_cmp_lg_u32 s5, 0
	s_cselect_b32 s8, s8, 0x14000
	s_add_i32 s8, s22, s8
	s_waitcnt lgkmcnt(0)
	s_barrier
	v_lshl_add_u64 v[10:11], v[200:201], 0, s[64:65]
	s_mov_b32 m0, s8
	s_nop 0
	global_load_lds_dwordx4 v[10:11], off
	v_lshl_add_u64 v[10:11], v[202:203], 0, s[64:65]
	s_add_i32 m0, s8, 0x400
	s_nop 0
	global_load_lds_dwordx4 v[10:11], off
	v_lshl_add_u64 v[10:11], v[204:205], 0, s[64:65]
	s_add_i32 m0, s8, 0x800
	s_nop 0
	global_load_lds_dwordx4 v[10:11], off
	v_lshl_add_u64 v[10:11], v[206:207], 0, s[64:65]
	s_add_i32 m0, s8, 0xc00
	s_nop 0
	global_load_lds_dwordx4 v[10:11], off
	v_lshl_add_u64 v[10:11], v[208:209], 0, s[64:65]
	s_add_i32 m0, s8, 0x1000
	s_lshl_b32 s64, s6, 18
	global_load_lds_dwordx4 v[10:11], off
	v_lshl_add_u64 v[10:11], v[210:211], 0, s[64:65]
	v_add_co_u32_e32 v14, vcc, s33, v10
	s_nop 1
	v_addc_co_u32_e32 v15, vcc, 0, v11, vcc
	global_load_dwordx4 v[10:13], v[10:11], off nt
	s_nop 0
	global_load_dwordx4 v[14:17], v[14:15], off nt
	v_add_u32_e32 v38, s7, v86
	ds_read2_b32 v[18:19], v232 offset0:0 offset1:0x84
	ds_read2_b32 v[20:21], v233 offset0:0 offset1:0x84
	ds_read2_b32 v[22:23], v232 offset0:16 offset1:0x94
	ds_read2_b32 v[24:25], v233 offset0:16 offset1:0x94
	ds_read2_b32 v[26:27], v232 offset0:32 offset1:0xa4
	ds_read2_b32 v[28:29], v233 offset0:32 offset1:0xa4
	ds_read2_b32 v[30:31], v232 offset0:48 offset1:0xb4
	ds_read2_b32 v[32:33], v233 offset0:48 offset1:0xb4
	ds_read_b128 v[34:37], v38 offset:0
	ds_read_b128 v[38:41], v38 offset:0x400
	s_nop 0
	s_waitcnt lgkmcnt(1)
	s_setprio 1
	v_mfma_f32_16x16x32_bf16 v[70:73], v[26:29], v[34:37], v[70:73]
	s_waitcnt lgkmcnt(0)
	v_mfma_f32_16x16x32_bf16 v[42:45], v[18:21], v[34:37], v[78:81]
	v_mfma_f32_16x16x32_bf16 v[46:49], v[22:25], v[34:37], v[74:77]
	v_mfma_f32_16x16x32_bf16 v[34:37], v[30:33], v[34:37], v[66:69]
	v_mfma_f32_16x16x32_bf16 v[18:21], v[18:21], v[38:41], v[62:65]
	v_mfma_f32_16x16x32_bf16 v[22:25], v[22:25], v[38:41], v[58:61]
	v_mfma_f32_16x16x32_bf16 v[26:29], v[26:29], v[38:41], v[54:57]
	v_mfma_f32_16x16x32_bf16 v[30:33], v[30:33], v[38:41], v[50:53]
	s_setprio 0
	s_add_i32 s6, s5, 1
	s_cmp_lg_u32 s5, 2
	s_cselect_b32 s5, s6, 0
	s_min_u32 s6, s4, 12
	s_add_i32 s6, s6, 3
	s_mul_i32 s7, s5, 0xa000
	s_lshl_b32 s64, s6, 6
	s_add_i32 s8, s7, 0xffff6000
	s_cmp_lg_u32 s5, 0
	s_waitcnt vmcnt(7)
	v_cvt_pk_bf16_f32 v2, v2, v6
	v_add_u32_e32 v6, 0x20100, v236
	s_cselect_b32 s8, s8, 0x14000
	v_cvt_pk_bf16_f32 v3, v3, v7
	v_cvt_pk_bf16_f32 v4, v4, v8
	v_cvt_pk_bf16_f32 v5, v5, v9
	ds_write_b128 v6, v[2:5]
	s_add_i32 s8, s22, s8
	s_waitcnt lgkmcnt(0)
	s_barrier
	v_lshl_add_u64 v[2:3], v[200:201], 0, s[64:65]
	s_mov_b32 m0, s8
	s_nop 0
	global_load_lds_dwordx4 v[2:3], off
	v_lshl_add_u64 v[2:3], v[202:203], 0, s[64:65]
	s_add_i32 m0, s8, 0x400
	s_nop 0
	global_load_lds_dwordx4 v[2:3], off
	v_lshl_add_u64 v[2:3], v[204:205], 0, s[64:65]
	s_add_i32 m0, s8, 0x800
	s_nop 0
	global_load_lds_dwordx4 v[2:3], off
	v_lshl_add_u64 v[2:3], v[206:207], 0, s[64:65]
	s_add_i32 m0, s8, 0xc00
	s_nop 0
	global_load_lds_dwordx4 v[2:3], off
	v_lshl_add_u64 v[2:3], v[208:209], 0, s[64:65]
	s_lshl_b32 s64, s6, 18
	s_add_i32 m0, s8, 0x1000
	v_lshl_add_u64 v[6:7], v[210:211], 0, s[64:65]
	global_load_lds_dwordx4 v[2:3], off
	global_load_dwordx4 v[2:5], v[6:7], off nt
	v_add_co_u32_e32 v6, vcc, s33, v6
	s_nop 1
	v_addc_co_u32_e32 v7, vcc, 0, v7, vcc
	global_load_dwordx4 v[6:9], v[6:7], off nt
	v_add_u32_e32 v62, s7, v86
	ds_read2_b32 v[38:39], v234 offset0:0 offset1:0x84
	ds_read2_b32 v[40:41], v235 offset0:0 offset1:0x84
	ds_read2_b32 v[50:51], v234 offset0:16 offset1:0x94
	ds_read2_b32 v[52:53], v235 offset0:16 offset1:0x94
	ds_read2_b32 v[54:55], v234 offset0:32 offset1:0xa4
	ds_read2_b32 v[56:57], v235 offset0:32 offset1:0xa4
	ds_read2_b32 v[82:83], v234 offset0:48 offset1:0xb4
	ds_read2_b32 v[84:85], v235 offset0:48 offset1:0xb4
	ds_read_b128 v[58:61], v62 offset:0
	ds_read_b128 v[88:91], v62 offset:0x400
	s_nop 0
	s_waitcnt lgkmcnt(1)
	s_setprio 1
	v_mfma_f32_16x16x32_bf16 v[78:81], v[38:41], v[58:61], v[42:45]
	s_waitcnt lgkmcnt(0)
	v_mfma_f32_16x16x32_bf16 v[74:77], v[50:53], v[58:61], v[46:49]
	v_mfma_f32_16x16x32_bf16 v[70:73], v[54:57], v[58:61], v[70:73]
	v_mfma_f32_16x16x32_bf16 v[66:69], v[82:85], v[58:61], v[34:37]
	v_mfma_f32_16x16x32_bf16 v[62:65], v[38:41], v[88:91], v[18:21]
	v_mfma_f32_16x16x32_bf16 v[58:61], v[50:53], v[88:91], v[22:25]
	v_mfma_f32_16x16x32_bf16 v[54:57], v[54:57], v[88:91], v[26:29]
	v_mfma_f32_16x16x32_bf16 v[50:53], v[82:85], v[88:91], v[30:33]
	s_setprio 0
	s_waitcnt vmcnt(7)
	s_add_i32 s6, s5, 1
	s_cmp_lg_u32 s5, 2
	s_cselect_b32 s5, s6, 0
	s_cmp_gt_u32 s4, 13
	s_mov_b32 s6, s4
	s_waitcnt vmcnt(7)
	v_cvt_pk_bf16_f32 v10, v10, v14
	v_cvt_pk_bf16_f32 v11, v11, v15
	v_cvt_pk_bf16_f32 v12, v12, v16
	v_cvt_pk_bf16_f32 v13, v13, v17
	ds_write_b128 v237, v[10:13]
	s_cbranch_scc0 .LBB0_3470
	s_waitcnt vmcnt(0)
	v_mov_b32_e32 v49, 0
	v_mov_b32_e32 v48, v49
	v_mov_b32_e32 v47, v49
	v_mov_b32_e32 v46, v49
	v_mov_b32_e32 v45, v49
	v_mov_b32_e32 v44, v49
	v_mov_b32_e32 v43, v49
	v_mov_b32_e32 v42, v49
	v_mov_b32_e32 v41, v49
	v_mov_b32_e32 v40, v49
	v_mov_b32_e32 v39, v49
	v_mov_b32_e32 v38, v49
	v_mov_b32_e32 v37, v49
	v_mov_b32_e32 v36, v49
	v_mov_b32_e32 v35, v49
	v_mov_b32_e32 v34, v49
	v_mov_b32_e32 v21, v49
	v_mov_b32_e32 v20, v49
	v_mov_b32_e32 v19, v49
	v_mov_b32_e32 v18, v49
	v_mov_b32_e32 v25, v49
	v_mov_b32_e32 v24, v49
	v_mov_b32_e32 v23, v49
	v_mov_b32_e32 v22, v49
	v_mov_b32_e32 v29, v49
	v_mov_b32_e32 v28, v49
	v_mov_b32_e32 v27, v49
	v_mov_b32_e32 v26, v49
	v_mov_b32_e32 v33, v49
	v_mov_b32_e32 v32, v49
	v_mov_b32_e32 v31, v49
	v_mov_b32_e32 v30, v49
	v_mov_b32_e32 v91, v49
	v_mov_b32_e32 v90, v49
	v_mov_b32_e32 v89, v49
	v_mov_b32_e32 v88, v49
	v_mov_b32_e32 v115, v49
	v_mov_b32_e32 v114, v49
	v_mov_b32_e32 v113, v49
	v_mov_b32_e32 v112, v49
	v_mov_b32_e32 v111, v49
	v_mov_b32_e32 v110, v49
	v_mov_b32_e32 v109, v49
	v_mov_b32_e32 v108, v49
	v_mov_b32_e32 v103, v49
	v_mov_b32_e32 v102, v49
	v_mov_b32_e32 v101, v49
	v_mov_b32_e32 v100, v49
	v_mov_b32_e32 v85, v49
	v_mov_b32_e32 v84, v49
	v_mov_b32_e32 v83, v49
	v_mov_b32_e32 v82, v49
	v_mov_b32_e32 v95, v49
	v_mov_b32_e32 v94, v49
	v_mov_b32_e32 v93, v49
	v_mov_b32_e32 v92, v49
	v_mov_b32_e32 v99, v49
	v_mov_b32_e32 v98, v49
	v_mov_b32_e32 v97, v49
	v_mov_b32_e32 v96, v49
	v_mov_b32_e32 v107, v49
	v_mov_b32_e32 v106, v49
	v_mov_b32_e32 v105, v49
	v_mov_b32_e32 v104, v49
	v_mov_b32_e32 v119, v49
	v_mov_b32_e32 v118, v49
	v_mov_b32_e32 v117, v49
	v_mov_b32_e32 v116, v49
	v_mov_b32_e32 v127, v49
	v_mov_b32_e32 v126, v49
	v_mov_b32_e32 v125, v49
	v_mov_b32_e32 v124, v49
	v_mov_b32_e32 v135, v49
	v_mov_b32_e32 v134, v49
	v_mov_b32_e32 v133, v49
	v_mov_b32_e32 v132, v49
	v_mov_b32_e32 v139, v49
	v_mov_b32_e32 v138, v49
	v_mov_b32_e32 v137, v49
	v_mov_b32_e32 v136, v49
	v_mov_b32_e32 v123, v49
	v_mov_b32_e32 v122, v49
	v_mov_b32_e32 v121, v49
	v_mov_b32_e32 v120, v49
	v_mov_b32_e32 v131, v49
	v_mov_b32_e32 v130, v49
	v_mov_b32_e32 v129, v49
	v_mov_b32_e32 v128, v49
	v_mov_b32_e32 v143, v49
	v_mov_b32_e32 v142, v49
	v_mov_b32_e32 v141, v49
	v_mov_b32_e32 v140, v49
	v_mov_b32_e32 v147, v49
	v_mov_b32_e32 v146, v49
	v_mov_b32_e32 v145, v49
	v_mov_b32_e32 v144, v49
	v_mov_b32_e32 v151, v49
	v_mov_b32_e32 v150, v49
	v_mov_b32_e32 v149, v49
	v_mov_b32_e32 v148, v49
	v_mov_b32_e32 v179, v49
	v_mov_b32_e32 v178, v49
	v_mov_b32_e32 v177, v49
	v_mov_b32_e32 v176, v49
	v_mov_b32_e32 v175, v49
	v_mov_b32_e32 v174, v49
	v_mov_b32_e32 v173, v49
	v_mov_b32_e32 v172, v49
	v_mov_b32_e32 v171, v49
	v_mov_b32_e32 v170, v49
	v_mov_b32_e32 v169, v49
	v_mov_b32_e32 v168, v49
	v_mov_b32_e32 v167, v49
	v_mov_b32_e32 v166, v49
	v_mov_b32_e32 v165, v49
	v_mov_b32_e32 v164, v49
	v_mov_b32_e32 v163, v49
	v_mov_b32_e32 v162, v49
	v_mov_b32_e32 v161, v49
	v_mov_b32_e32 v160, v49
	v_mov_b32_e32 v159, v49
	v_mov_b32_e32 v158, v49
	v_mov_b32_e32 v157, v49
	v_mov_b32_e32 v156, v49
	v_mov_b32_e32 v155, v49
	v_mov_b32_e32 v154, v49
	v_mov_b32_e32 v153, v49
	v_mov_b32_e32 v152, v49
